# attention loops: canonicalizing self-max pairs around the row-max reduction and +0 row-sum adds removed (XDL->VALU distances re-padded); on top of v16
# baseline (speedup 1.0000x reference)
.LBB0_530:
	v_add_co_u32_e64 v0, s[42:43], s23, 3
	s_nop 0
	v_readfirstlane_b32 s26, v0
	s_add_i32 s27, s64, s8
	v_add_u32_e32 v0, s44, v226
	ds_read_b64_tr_b16 v[192:193], v0 offset:24576
	ds_read_b64_tr_b16 v[194:195], v0 offset:25088
	s_waitcnt lgkmcnt(9)
	v_mfma_f32_32x32x16_bf16 v[112:127], v[188:191], v[156:159], v[48:63]
	v_add_f32_e32 v2, v80, v81
	v_add_f32_e32 v2, v82, v2
	v_add_f32_e32 v2, v83, v2
	v_add_f32_e32 v2, v84, v2
	v_add_f32_e32 v2, v85, v2
	v_cvt_pk_bf16_f32 v140, v80, v81
	v_cvt_pk_bf16_f32 v141, v82, v83
	ds_read_b64_tr_b16 v[10:11], v0 offset:28672
	ds_read_b64_tr_b16 v[12:13], v0 offset:29184
	s_waitcnt lgkmcnt(10)
	v_mfma_f32_32x32x16_bf16 v[96:111], v[184:187], v[156:159], v[48:63]
	v_add_f32_e32 v2, v86, v2
	v_add_f32_e32 v2, v87, v2
	v_add_f32_e32 v2, v88, v2
	v_add_f32_e32 v6, v89, v2
	v_cvt_pk_bf16_f32 v142, v84, v85
	v_cvt_pk_bf16_f32 v143, v86, v87
	ds_read_b64_tr_b16 v[2:3], v0 offset:25600
	ds_read_b64_tr_b16 v[4:5], v0 offset:26112
	s_waitcnt lgkmcnt(11)
	v_mfma_f32_32x32x16_bf16 v[112:127], v[180:183], v[152:155], v[112:127]
	v_add_f32_e32 v6, v90, v6
	v_add_f32_e32 v6, v91, v6
	v_add_f32_e32 v6, v92, v6
	v_add_f32_e32 v14, v93, v6
	v_cvt_pk_bf16_f32 v136, v88, v89
	v_cvt_pk_bf16_f32 v137, v90, v91
	ds_read_b64_tr_b16 v[6:7], v0 offset:29696
	ds_read_b64_tr_b16 v[8:9], v0 offset:30208
	s_waitcnt lgkmcnt(12)
	v_mfma_f32_32x32x16_bf16 v[96:111], v[176:179], v[152:155], v[96:111]
	v_add_f32_e32 v14, v94, v14
	v_add_f32_e32 v14, v95, v14
	v_add_f32_e32 v14, v64, v14
	v_add_f32_e32 v14, v65, v14
	v_cvt_pk_bf16_f32 v138, v92, v93
	v_cvt_pk_bf16_f32 v139, v94, v95
	ds_read_b64_tr_b16 v[80:81], v0 offset:26624
	ds_read_b64_tr_b16 v[82:83], v0 offset:27136
	s_waitcnt lgkmcnt(13)
	v_mfma_f32_32x32x16_bf16 v[112:127], v[172:175], v[148:151], v[112:127]
	v_add_f32_e32 v14, v66, v14
	v_add_f32_e32 v14, v67, v14
	v_add_f32_e32 v14, v68, v14
	v_add_f32_e32 v14, v69, v14
	v_cvt_pk_bf16_f32 v132, v64, v65
	v_cvt_pk_bf16_f32 v133, v66, v67
	ds_read_b64_tr_b16 v[84:85], v0 offset:30720
	ds_read_b64_tr_b16 v[86:87], v0 offset:31232
	s_waitcnt lgkmcnt(14)
	v_mfma_f32_32x32x16_bf16 v[96:111], v[168:171], v[148:151], v[96:111]
	v_add_f32_e32 v14, v70, v14
	v_add_f32_e32 v14, v71, v14
	v_add_f32_e32 v14, v72, v14
	v_add_f32_e32 v14, v73, v14
	v_cvt_pk_bf16_f32 v134, v68, v69
	v_cvt_pk_bf16_f32 v135, v70, v71
	ds_read_b64_tr_b16 v[88:89], v0 offset:27648
	ds_read_b64_tr_b16 v[90:91], v0 offset:28160
	s_waitcnt lgkmcnt(14)
	v_mfma_f32_32x32x16_bf16 v[112:127], v[164:167], v[144:147], v[112:127]
	v_add_f32_e32 v14, v74, v14
	v_add_f32_e32 v14, v75, v14
	v_add_f32_e32 v14, v76, v14
	v_add_f32_e32 v14, v77, v14
	v_cvt_pk_bf16_f32 v128, v72, v73
	v_cvt_pk_bf16_f32 v129, v74, v75
	ds_read_b64_tr_b16 v[92:93], v0 offset:31744
	ds_read_b64_tr_b16 v[94:95], v0 offset:32256
	v_mfma_f32_32x32x16_bf16 v[96:111], v[160:163], v[144:147], v[96:111]
	v_add_f32_e32 v0, v78, v14
	v_add_f32_e32 v0, v79, v0
	v_cvt_pk_bf16_f32 v130, v76, v77
	v_cvt_pk_bf16_f32 v131, v78, v79
	s_mov_b32 s44, m0
	s_mov_b32 m0, s27
	s_nop 0
	global_load_lds_dwordx4 v[198:199], off
	s_mov_b32 m0, s44
	s_andn2_b64 vcc, exec, s[42:43]
	s_mov_b64 s[44:45], -1
	s_cbranch_vccz .LBB0_532
	s_add_i32 s68, s23, s1
	s_lshl_b64 s[42:43], s[68:69], 6
	s_add_u32 s42, s42, s33
	s_addc_u32 s43, s43, 0
	s_mov_b64 s[44:45], 0

.LBB0_568:
	v_max_f32_e32 v14, v112, v113
	v_max3_f32 v15, v114, v115, v97
	v_max3_f32 v14, v14, v96, v98
	v_max3_f32 v14, v14, v99, v116
	v_max3_f32 v15, v15, v118, v119
	v_max3_f32 v14, v14, v117, v100
	v_max3_f32 v15, v15, v102, v103
	v_max3_f32 v14, v14, v101, v120
	v_max3_f32 v15, v15, v122, v123
	v_max3_f32 v14, v14, v121, v104
	v_max3_f32 v15, v15, v106, v107
	v_max3_f32 v14, v14, v105, v124
	v_max3_f32 v15, v15, v126, v127
	v_max3_f32 v14, v14, v125, v108
	v_max3_f32 v15, v15, v110, v111
	v_max3_f32 v14, v14, v109, v15
	v_mov_b32_e32 v15, v14
	s_nop 1
	v_permlane32_swap_b32_e32 v14, v15
	v_max_f32_e32 v14, v14, v15
	v_cmp_lt_f32_e32 vcc, s22, v14
	s_cmp_lg_u64 vcc, 0
	v_add_f32_e32 v0, v229, v0
	s_cselect_b64 s[42:43], -1, 0
	s_cbranch_vccnz .LBB0_612

.LBB0_571:
	v_add_u32_e32 v14, s64, v226
	ds_read_b64_tr_b16 v[160:161], v14 offset:24576
	ds_read_b64_tr_b16 v[162:163], v14 offset:25088
	s_waitcnt lgkmcnt(9)
	v_mfma_f32_32x32x16_bf16 v[80:95], v[64:67], v[156:159], v[48:63]
	v_add_f32_e32 v2, v112, v113
	v_add_f32_e32 v2, v114, v2
	v_add_f32_e32 v2, v115, v2
	v_add_f32_e32 v2, v116, v2
	v_add_f32_e32 v2, v117, v2
	v_cvt_pk_bf16_f32 v140, v112, v113
	v_cvt_pk_bf16_f32 v141, v114, v115
	ds_read_b64_tr_b16 v[112:113], v14 offset:28672
	ds_read_b64_tr_b16 v[114:115], v14 offset:29184
	s_waitcnt lgkmcnt(10)
	v_mfma_f32_32x32x16_bf16 v[64:79], v[180:183], v[156:159], v[48:63]
	v_add_f32_e32 v2, v118, v2
	v_add_f32_e32 v2, v119, v2
	v_add_f32_e32 v2, v120, v2
	v_add_f32_e32 v6, v121, v2
	v_cvt_pk_bf16_f32 v142, v116, v117
	v_cvt_pk_bf16_f32 v143, v118, v119
	ds_read_b64_tr_b16 v[2:3], v14 offset:25600
	ds_read_b64_tr_b16 v[4:5], v14 offset:26112
	s_waitcnt lgkmcnt(11)
	v_mfma_f32_32x32x16_bf16 v[80:95], v[184:187], v[152:155], v[80:95]
	v_add_f32_e32 v6, v122, v6
	v_add_f32_e32 v6, v123, v6
	v_add_f32_e32 v6, v124, v6
	v_add_f32_e32 v15, v125, v6
	v_cvt_pk_bf16_f32 v136, v120, v121
	v_cvt_pk_bf16_f32 v137, v122, v123
	ds_read_b64_tr_b16 v[6:7], v14 offset:29696
	ds_read_b64_tr_b16 v[8:9], v14 offset:30208
	s_waitcnt lgkmcnt(12)
	v_mfma_f32_32x32x16_bf16 v[64:79], v[10:13], v[152:155], v[64:79]
	v_add_f32_e32 v10, v126, v15
	v_add_f32_e32 v10, v127, v10
	v_add_f32_e32 v10, v96, v10
	v_add_f32_e32 v15, v97, v10
	v_cvt_pk_bf16_f32 v138, v124, v125
	v_cvt_pk_bf16_f32 v139, v126, v127
	ds_read_b64_tr_b16 v[10:11], v14 offset:26624
	ds_read_b64_tr_b16 v[12:13], v14 offset:27136
	s_waitcnt lgkmcnt(13)
	v_mfma_f32_32x32x16_bf16 v[80:95], v[176:179], v[148:151], v[80:95]
	v_add_f32_e32 v15, v98, v15
	v_add_f32_e32 v15, v99, v15
	v_add_f32_e32 v15, v100, v15
	v_add_f32_e32 v15, v101, v15
	v_cvt_pk_bf16_f32 v132, v96, v97
	v_cvt_pk_bf16_f32 v133, v98, v99
	ds_read_b64_tr_b16 v[116:117], v14 offset:30720
	ds_read_b64_tr_b16 v[118:119], v14 offset:31232
	s_waitcnt lgkmcnt(14)
	v_mfma_f32_32x32x16_bf16 v[64:79], v[172:175], v[148:151], v[64:79]
	v_add_f32_e32 v15, v102, v15
	v_add_f32_e32 v15, v103, v15
	v_add_f32_e32 v15, v104, v15
	v_add_f32_e32 v15, v105, v15
	v_cvt_pk_bf16_f32 v134, v100, v101
	v_cvt_pk_bf16_f32 v135, v102, v103
	ds_read_b64_tr_b16 v[120:121], v14 offset:27648
	ds_read_b64_tr_b16 v[122:123], v14 offset:28160
	s_waitcnt lgkmcnt(14)
	v_mfma_f32_32x32x16_bf16 v[80:95], v[168:171], v[144:147], v[80:95]
	v_add_f32_e32 v15, v106, v15
	v_add_f32_e32 v15, v107, v15
	v_add_f32_e32 v15, v108, v15
	v_add_f32_e32 v15, v109, v15
	v_cvt_pk_bf16_f32 v128, v104, v105
	v_cvt_pk_bf16_f32 v129, v106, v107
	ds_read_b64_tr_b16 v[124:125], v14 offset:31744
	ds_read_b64_tr_b16 v[126:127], v14 offset:32256
	v_mfma_f32_32x32x16_bf16 v[64:79], v[164:167], v[144:147], v[64:79]
	v_add_f32_e32 v14, v110, v15
	v_add_f32_e32 v14, v111, v14
	v_cvt_pk_bf16_f32 v130, v108, v109
	v_cvt_pk_bf16_f32 v131, v110, v111
	s_mov_b64 s[42:43], 0xd8000
	v_lshl_add_u64 v[96:97], v[198:199], 0, s[42:43]
	s_add_i32 s27, s47, s8
	s_mov_b32 s42, m0
	s_mov_b32 m0, s27
	s_nop 0
	global_load_lds_dwordx4 v[96:97], off
	s_mov_b32 m0, s42
	s_cmp_lt_u32 s26, 2
	s_mov_b64 s[42:43], s[6:7]
	s_cbranch_scc1 .LBB0_573
	s_add_i32 s27, s23, s1
	s_add_i32 s68, s27, 1
	s_lshl_b64 s[42:43], s[68:69], 6
	s_add_u32 s42, s42, s33
	s_addc_u32 s43, s43, 0

.LBB0_607:
	v_add_f32_e32 v229, v0, v14
	v_max_f32_e32 v0, v80, v81
	v_max3_f32 v14, v82, v83, v65
	v_max3_f32 v0, v0, v64, v66
	v_max3_f32 v0, v0, v67, v84
	v_max3_f32 v14, v14, v86, v87
	v_max3_f32 v0, v0, v85, v68
	v_max3_f32 v14, v14, v70, v71
	v_max3_f32 v0, v0, v69, v88
	v_max3_f32 v14, v14, v90, v91
	v_max3_f32 v0, v0, v89, v72
	v_max3_f32 v14, v14, v74, v75
	v_max3_f32 v0, v0, v73, v92
	v_max3_f32 v14, v14, v94, v95
	v_max3_f32 v0, v0, v93, v76
	v_max3_f32 v14, v14, v78, v79
	v_max3_f32 v0, v0, v77, v14
	v_mov_b32_e32 v14, v0
	s_nop 1
	v_permlane32_swap_b32_e32 v0, v14
	v_max_f32_e32 v0, v0, v14
	v_cmp_lt_f32_e32 vcc, s22, v0
	s_cmp_lg_u64 vcc, 0
	s_cselect_b64 s[42:43], -1, 0
	s_cbranch_vccnz .LBB0_615

.LBB0_621:
	s_add_i32 s50, s23, s75
	v_add_u32_e32 v0, s47, v226
	ds_read_b64_tr_b16 v[192:193], v0 offset:24576
	ds_read_b64_tr_b16 v[194:195], v0 offset:25088
	s_waitcnt lgkmcnt(9)
	v_mfma_f32_32x32x16_bf16 v[112:127], v[188:191], v[156:159], v[48:63]
	v_add_f32_e32 v2, v80, v81
	v_add_f32_e32 v2, v82, v2
	v_add_f32_e32 v2, v83, v2
	v_add_f32_e32 v2, v84, v2
	v_add_f32_e32 v2, v85, v2
	v_cvt_pk_bf16_f32 v140, v80, v81
	v_cvt_pk_bf16_f32 v141, v82, v83
	ds_read_b64_tr_b16 v[80:81], v0 offset:28672
	ds_read_b64_tr_b16 v[82:83], v0 offset:29184
	s_waitcnt lgkmcnt(10)
	v_mfma_f32_32x32x16_bf16 v[96:111], v[184:187], v[156:159], v[48:63]
	v_add_f32_e32 v2, v86, v2
	v_add_f32_e32 v2, v87, v2
	v_add_f32_e32 v2, v88, v2
	v_add_f32_e32 v6, v89, v2
	v_cvt_pk_bf16_f32 v142, v84, v85
	v_cvt_pk_bf16_f32 v143, v86, v87
	ds_read_b64_tr_b16 v[2:3], v0 offset:25600
	ds_read_b64_tr_b16 v[4:5], v0 offset:26112
	s_waitcnt lgkmcnt(11)
	v_mfma_f32_32x32x16_bf16 v[112:127], v[180:183], v[152:155], v[112:127]
	v_add_f32_e32 v6, v90, v6
	v_add_f32_e32 v6, v91, v6
	v_add_f32_e32 v6, v92, v6
	v_add_f32_e32 v10, v93, v6
	v_cvt_pk_bf16_f32 v136, v88, v89
	v_cvt_pk_bf16_f32 v137, v90, v91
	ds_read_b64_tr_b16 v[6:7], v0 offset:29696
	ds_read_b64_tr_b16 v[8:9], v0 offset:30208
	s_waitcnt lgkmcnt(12)
	v_mfma_f32_32x32x16_bf16 v[96:111], v[176:179], v[152:155], v[96:111]
	v_add_f32_e32 v10, v94, v10
	v_add_f32_e32 v10, v95, v10
	v_add_f32_e32 v10, v64, v10
	v_add_f32_e32 v84, v65, v10
	v_cvt_pk_bf16_f32 v138, v92, v93
	v_cvt_pk_bf16_f32 v139, v94, v95
	ds_read_b64_tr_b16 v[10:11], v0 offset:26624
	ds_read_b64_tr_b16 v[12:13], v0 offset:27136
	s_waitcnt lgkmcnt(13)
	v_mfma_f32_32x32x16_bf16 v[112:127], v[172:175], v[148:151], v[112:127]
	v_add_f32_e32 v84, v66, v84
	v_add_f32_e32 v84, v67, v84
	v_add_f32_e32 v84, v68, v84
	v_add_f32_e32 v88, v69, v84
	v_cvt_pk_bf16_f32 v132, v64, v65
	v_cvt_pk_bf16_f32 v133, v66, v67
	ds_read_b64_tr_b16 v[84:85], v0 offset:30720
	ds_read_b64_tr_b16 v[86:87], v0 offset:31232
	s_waitcnt lgkmcnt(14)
	v_mfma_f32_32x32x16_bf16 v[96:111], v[168:171], v[148:151], v[96:111]
	v_add_f32_e32 v64, v70, v88
	v_add_f32_e32 v64, v71, v64
	v_add_f32_e32 v64, v72, v64
	v_add_f32_e32 v64, v73, v64
	v_cvt_pk_bf16_f32 v134, v68, v69
	v_cvt_pk_bf16_f32 v135, v70, v71
	ds_read_b64_tr_b16 v[88:89], v0 offset:27648
	ds_read_b64_tr_b16 v[90:91], v0 offset:28160
	s_waitcnt lgkmcnt(14)
	v_mfma_f32_32x32x16_bf16 v[112:127], v[164:167], v[144:147], v[112:127]
	v_add_f32_e32 v64, v74, v64
	v_add_f32_e32 v64, v75, v64
	v_add_f32_e32 v64, v76, v64
	v_add_f32_e32 v64, v77, v64
	v_cvt_pk_bf16_f32 v128, v72, v73
	v_cvt_pk_bf16_f32 v129, v74, v75
	ds_read_b64_tr_b16 v[92:93], v0 offset:31744
	ds_read_b64_tr_b16 v[94:95], v0 offset:32256
	v_mfma_f32_32x32x16_bf16 v[96:111], v[160:163], v[144:147], v[96:111]
	v_add_f32_e32 v0, v78, v64
	v_add_f32_e32 v0, v79, v0
	v_cvt_pk_bf16_f32 v130, v76, v77
	v_cvt_pk_bf16_f32 v131, v78, v79
	s_cmp_ge_i32 s50, s88
	s_cselect_b64 s[44:45], -1, 0
	s_and_b64 vcc, exec, s[44:45]
	s_cbranch_vccnz .LBB0_623
	s_add_i32 s6, s64, s8
	s_mov_b32 s7, m0
	s_mov_b32 m0, s6
	s_nop 0
	global_load_lds_dwordx4 v[206:207], off
	s_mov_b32 m0, s7

.LBB0_659:
	v_max_f32_e32 v64, v112, v113
	v_max3_f32 v65, v114, v115, v97
	v_max3_f32 v64, v64, v96, v98
	v_max3_f32 v64, v64, v99, v116
	v_max3_f32 v65, v65, v118, v119
	v_max3_f32 v64, v64, v117, v100
	v_max3_f32 v65, v65, v102, v103
	v_max3_f32 v64, v64, v101, v120
	v_max3_f32 v65, v65, v122, v123
	v_max3_f32 v64, v64, v121, v104
	v_max3_f32 v65, v65, v106, v107
	v_max3_f32 v64, v64, v105, v124
	v_max3_f32 v65, v65, v126, v127
	v_max3_f32 v64, v64, v125, v108
	v_max3_f32 v65, v65, v110, v111
	v_max3_f32 v64, v64, v109, v65
	v_mov_b32_e32 v65, v64
	s_nop 1
	v_permlane32_swap_b32_e32 v64, v65
	v_max_f32_e32 v64, v64, v65
	v_cmp_lt_f32_e32 vcc, s22, v64
	s_cmp_lg_u64 vcc, 0
	v_add_f32_e32 v0, v229, v0
	s_cselect_b64 s[6:7], -1, 0
	s_cbranch_vccnz .LBB0_729

.LBB0_706:
	v_add_f32_e32 v229, v0, v120
	v_max_f32_e32 v0, v80, v81
	v_max3_f32 v96, v82, v83, v65
	v_max3_f32 v0, v0, v64, v66
	v_max3_f32 v0, v0, v67, v84
	v_max3_f32 v96, v96, v86, v87
	v_max3_f32 v0, v0, v85, v68
	v_max3_f32 v96, v96, v70, v71
	v_max3_f32 v0, v0, v69, v88
	v_max3_f32 v96, v96, v90, v91
	v_max3_f32 v0, v0, v89, v72
	v_max3_f32 v96, v96, v74, v75
	v_max3_f32 v0, v0, v73, v92
	v_max3_f32 v96, v96, v94, v95
	v_max3_f32 v0, v0, v93, v76
	v_max3_f32 v96, v96, v78, v79
	v_max3_f32 v0, v0, v77, v96
	v_mov_b32_e32 v96, v0
	s_nop 1
	v_permlane32_swap_b32_e32 v0, v96
	v_max_f32_e32 v0, v0, v96
	v_cmp_lt_f32_e32 vcc, s22, v0
	s_cmp_lg_u64 vcc, 0
	s_cselect_b64 s[50:51], -1, 0
	s_cbranch_vccnz .LBB0_732

.LBB0_737:
	v_add_u32_e32 v0, s81, v226
	ds_read_b64_tr_b16 v[6:7], v0 offset:24576
	ds_read_b64_tr_b16 v[8:9], v0 offset:25088
	s_waitcnt lgkmcnt(9)
	v_mfma_f32_32x32x16_bf16 v[96:111], v[188:191], v[156:159], v[48:63]
	v_add_f32_e32 v2, v80, v81
	v_add_f32_e32 v2, v82, v2
	v_add_f32_e32 v2, v83, v2
	v_add_f32_e32 v2, v84, v2
	v_add_f32_e32 v10, v85, v2
	v_cvt_pk_bf16_f32 v140, v80, v81
	v_cvt_pk_bf16_f32 v141, v82, v83
	ds_read_b64_tr_b16 v[2:3], v0 offset:28672
	ds_read_b64_tr_b16 v[4:5], v0 offset:29184
	s_waitcnt lgkmcnt(10)
	v_mfma_f32_32x32x16_bf16 v[48:63], v[184:187], v[156:159], v[48:63]
	v_add_f32_e32 v10, v86, v10
	v_add_f32_e32 v10, v87, v10
	v_add_f32_e32 v10, v88, v10
	v_add_f32_e32 v14, v89, v10
	v_cvt_pk_bf16_f32 v142, v84, v85
	v_cvt_pk_bf16_f32 v143, v86, v87
	ds_read_b64_tr_b16 v[10:11], v0 offset:25600
	ds_read_b64_tr_b16 v[12:13], v0 offset:26112
	s_waitcnt lgkmcnt(11)
	v_mfma_f32_32x32x16_bf16 v[96:111], v[180:183], v[152:155], v[96:111]
	v_add_f32_e32 v14, v90, v14
	v_add_f32_e32 v14, v91, v14
	v_add_f32_e32 v14, v92, v14
	v_add_f32_e32 v14, v93, v14
	v_cvt_pk_bf16_f32 v136, v88, v89
	v_cvt_pk_bf16_f32 v137, v90, v91
	ds_read_b64_tr_b16 v[80:81], v0 offset:29696
	ds_read_b64_tr_b16 v[82:83], v0 offset:30208
	s_waitcnt lgkmcnt(12)
	v_mfma_f32_32x32x16_bf16 v[48:63], v[176:179], v[152:155], v[48:63]
	v_add_f32_e32 v14, v94, v14
	v_add_f32_e32 v14, v95, v14
	v_add_f32_e32 v14, v64, v14
	v_add_f32_e32 v14, v65, v14
	v_cvt_pk_bf16_f32 v138, v92, v93
	v_cvt_pk_bf16_f32 v139, v94, v95
	ds_read_b64_tr_b16 v[84:85], v0 offset:26624
	ds_read_b64_tr_b16 v[86:87], v0 offset:27136
	s_waitcnt lgkmcnt(13)
	v_mfma_f32_32x32x16_bf16 v[96:111], v[172:175], v[148:151], v[96:111]
	v_add_f32_e32 v14, v66, v14
	v_add_f32_e32 v14, v67, v14
	v_add_f32_e32 v14, v68, v14
	v_add_f32_e32 v14, v69, v14
	v_cvt_pk_bf16_f32 v132, v64, v65
	v_cvt_pk_bf16_f32 v133, v66, v67
	ds_read_b64_tr_b16 v[88:89], v0 offset:30720
	ds_read_b64_tr_b16 v[90:91], v0 offset:31232
	s_waitcnt lgkmcnt(14)
	v_mfma_f32_32x32x16_bf16 v[48:63], v[168:171], v[148:151], v[48:63]
	v_add_f32_e32 v14, v70, v14
	v_add_f32_e32 v14, v71, v14
	v_add_f32_e32 v14, v72, v14
	v_add_f32_e32 v14, v73, v14
	v_cvt_pk_bf16_f32 v134, v68, v69
	v_cvt_pk_bf16_f32 v135, v70, v71
	ds_read_b64_tr_b16 v[92:93], v0 offset:27648
	ds_read_b64_tr_b16 v[94:95], v0 offset:28160
	s_waitcnt lgkmcnt(14)
	v_mfma_f32_32x32x16_bf16 v[96:111], v[164:167], v[144:147], v[96:111]
	v_add_f32_e32 v14, v74, v14
	v_add_f32_e32 v14, v75, v14
	v_add_f32_e32 v14, v76, v14
	v_add_f32_e32 v14, v77, v14
	v_cvt_pk_bf16_f32 v128, v72, v73
	v_cvt_pk_bf16_f32 v129, v74, v75
	ds_read_b64_tr_b16 v[112:113], v0 offset:31744
	ds_read_b64_tr_b16 v[114:115], v0 offset:32256
	v_mfma_f32_32x32x16_bf16 v[48:63], v[160:163], v[144:147], v[48:63]
	v_add_f32_e32 v0, v78, v14
	v_add_f32_e32 v0, v79, v0
	v_cvt_pk_bf16_f32 v130, v76, v77
	v_cvt_pk_bf16_f32 v131, v78, v79
	s_cmp_lt_i32 s0, 5
	s_cbranch_scc1 .LBB0_771
	s_add_i32 s65, s65, s63
	s_max_i32 s0, s65, 4
	s_add_i32 s0, s0, -4
	s_min_u32 s0, s0, 56
	s_add_i32 s13, s13, s12
	s_sub_i32 s0, s13, s0
	s_cmp_gt_u32 s0, 7
	s_cselect_b64 vcc, -1, 0
	s_cbranch_scc1 .Lna_allmask_4
	s_sub_i32 s0, s13, s65
	s_max_i32 s0, s0, -7
	s_add_i32 s0, s0, 7
	s_min_u32 s0, s0, 14
	s_mulk_i32 s0, 0x7c
	v_lshlrev_b32_e32 v14, 2, v224
	v_add3_u32 v116, v225, s0, v14
	v_lshlrev_b32_e32 v76, 2, v223
	v_add_u32_e32 v76, 0x16100, v76
	ds_read_b32 v64, v116
	ds_read_b32 v70, v76
	ds_read_b32 v65, v116 offset:4
	ds_read_b32 v71, v76 offset:4
	ds_read_b32 v66, v116 offset:8
	ds_read_b32 v72, v76 offset:8
	ds_read_b32 v67, v116 offset:12
	ds_read_b32 v73, v76 offset:12
	ds_read_b32 v68, v116 offset:32
	ds_read_b32 v74, v76 offset:32
	ds_read_b32 v69, v116 offset:36
	ds_read_b32 v75, v76 offset:36
	s_waitcnt lgkmcnt(10)
	v_add_f32_e32 v96, v96, v64
	v_add_f32_e32 v96, v96, v70
	ds_read_b32 v64, v116 offset:40
	ds_read_b32 v70, v76 offset:40
	s_waitcnt lgkmcnt(10)
	v_add_f32_e32 v97, v97, v65
	v_add_f32_e32 v97, v97, v71
	ds_read_b32 v65, v116 offset:44
	ds_read_b32 v71, v76 offset:44
	s_waitcnt lgkmcnt(10)
	v_add_f32_e32 v98, v98, v66
	v_add_f32_e32 v98, v98, v72
	ds_read_b32 v66, v116 offset:64
	ds_read_b32 v72, v76 offset:64
	s_waitcnt lgkmcnt(10)
	v_add_f32_e32 v99, v99, v67
	v_add_f32_e32 v99, v99, v73
	ds_read_b32 v67, v116 offset:68
	ds_read_b32 v73, v76 offset:68
	s_waitcnt lgkmcnt(10)
	v_add_f32_e32 v100, v100, v68
	v_add_f32_e32 v100, v100, v74
	ds_read_b32 v68, v116 offset:72
	ds_read_b32 v74, v76 offset:72
	s_waitcnt lgkmcnt(10)
	v_add_f32_e32 v101, v101, v69
	v_add_f32_e32 v101, v101, v75
	ds_read_b32 v69, v116 offset:76
	ds_read_b32 v75, v76 offset:76
	s_waitcnt lgkmcnt(10)
	v_add_f32_e32 v102, v102, v64
	v_add_f32_e32 v102, v102, v70
	ds_read_b32 v64, v116 offset:96
	ds_read_b32 v70, v76 offset:96
	s_waitcnt lgkmcnt(10)
	v_add_f32_e32 v103, v103, v65
	v_add_f32_e32 v103, v103, v71
	ds_read_b32 v65, v116 offset:100
	ds_read_b32 v71, v76 offset:100
	s_waitcnt lgkmcnt(10)
	v_add_f32_e32 v104, v104, v66
	v_add_f32_e32 v104, v104, v72
	ds_read_b32 v66, v116 offset:104
	ds_read_b32 v72, v76 offset:104
	s_waitcnt lgkmcnt(10)
	v_add_f32_e32 v105, v105, v67
	v_add_f32_e32 v105, v105, v73
	ds_read_b32 v67, v116 offset:108
	ds_read_b32 v73, v76 offset:108
	s_waitcnt lgkmcnt(10)
	v_add_f32_e32 v106, v106, v68
	v_add_f32_e32 v106, v106, v74
	ds_read_b32 v68, v116 offset:128
	ds_read_b32 v74, v76 offset:128
	s_waitcnt lgkmcnt(10)
	v_add_f32_e32 v107, v107, v69
	v_add_f32_e32 v107, v107, v75
	ds_read_b32 v69, v116 offset:132
	ds_read_b32 v75, v76 offset:132
	s_waitcnt lgkmcnt(10)
	v_add_f32_e32 v108, v108, v64
	v_add_f32_e32 v108, v108, v70
	ds_read_b32 v64, v116 offset:136
	ds_read_b32 v70, v76 offset:136
	s_waitcnt lgkmcnt(10)
	v_add_f32_e32 v109, v109, v65
	v_add_f32_e32 v109, v109, v71
	ds_read_b32 v65, v116 offset:140
	ds_read_b32 v71, v76 offset:140
	s_waitcnt lgkmcnt(10)
	v_add_f32_e32 v110, v110, v66
	v_add_f32_e32 v110, v110, v72
	ds_read_b32 v66, v116 offset:160
	ds_read_b32 v72, v76 offset:160
	s_waitcnt lgkmcnt(10)
	v_add_f32_e32 v111, v111, v67
	v_add_f32_e32 v111, v111, v73
	ds_read_b32 v67, v116 offset:164
	ds_read_b32 v73, v76 offset:164
	s_waitcnt lgkmcnt(10)
	v_add_f32_e32 v48, v48, v68
	v_add_f32_e32 v48, v48, v74
	ds_read_b32 v68, v116 offset:168
	ds_read_b32 v74, v76 offset:168
	s_waitcnt lgkmcnt(10)
	v_add_f32_e32 v49, v49, v69
	v_add_f32_e32 v49, v49, v75
	ds_read_b32 v69, v116 offset:172
	ds_read_b32 v75, v76 offset:172
	s_waitcnt lgkmcnt(10)
	v_add_f32_e32 v50, v50, v64
	v_add_f32_e32 v50, v50, v70
	ds_read_b32 v64, v116 offset:192
	ds_read_b32 v70, v76 offset:192
	s_waitcnt lgkmcnt(10)
	v_add_f32_e32 v51, v51, v65
	v_add_f32_e32 v51, v51, v71
	ds_read_b32 v65, v116 offset:196
	ds_read_b32 v71, v76 offset:196
	s_waitcnt lgkmcnt(10)
	v_add_f32_e32 v52, v52, v66
	v_add_f32_e32 v52, v52, v72
	ds_read_b32 v66, v116 offset:200
	ds_read_b32 v72, v76 offset:200
	s_waitcnt lgkmcnt(10)
	v_add_f32_e32 v53, v53, v67
	v_add_f32_e32 v53, v53, v73
	ds_read_b32 v67, v116 offset:204
	ds_read_b32 v73, v76 offset:204
	s_waitcnt lgkmcnt(10)
	v_add_f32_e32 v54, v54, v68
	v_add_f32_e32 v54, v54, v74
	ds_read_b32 v68, v116 offset:224
	ds_read_b32 v74, v76 offset:224
	s_waitcnt lgkmcnt(10)
	v_add_f32_e32 v55, v55, v69
	v_add_f32_e32 v55, v55, v75
	ds_read_b32 v69, v116 offset:228
	ds_read_b32 v75, v76 offset:228
	s_waitcnt lgkmcnt(10)
	v_add_f32_e32 v56, v56, v64
	v_add_f32_e32 v56, v56, v70
	ds_read_b32 v64, v116 offset:232
	ds_read_b32 v70, v76 offset:232
	s_waitcnt lgkmcnt(10)
	v_add_f32_e32 v57, v57, v65
	v_add_f32_e32 v57, v57, v71
	ds_read_b32 v65, v116 offset:236
	ds_read_b32 v71, v76 offset:236
	s_waitcnt lgkmcnt(10)
	v_add_f32_e32 v58, v58, v66
	v_add_f32_e32 v58, v58, v72
	s_waitcnt lgkmcnt(8)
	v_add_f32_e32 v59, v59, v67
	v_add_f32_e32 v59, v59, v73
	s_waitcnt lgkmcnt(6)
	v_add_f32_e32 v60, v60, v68
	v_add_f32_e32 v60, v60, v74
	s_waitcnt lgkmcnt(4)
	v_add_f32_e32 v61, v61, v69
	v_add_f32_e32 v61, v61, v75
	s_waitcnt lgkmcnt(2)
	v_add_f32_e32 v62, v62, v64
	v_add_f32_e32 v62, v62, v70
	s_waitcnt lgkmcnt(0)
	v_add_f32_e32 v63, v63, v65
	v_add_f32_e32 v63, v63, v71
	s_branch .LBB0_771

.LBB0_771:
	v_max_f32_e32 v14, v96, v97
	s_nop 1
	v_max3_f32 v15, v98, v99, v49
	v_max3_f32 v14, v14, v48, v50
	v_max3_f32 v14, v14, v51, v100
	v_max3_f32 v15, v15, v102, v103
	v_max3_f32 v14, v14, v101, v52
	v_max3_f32 v15, v15, v54, v55
	v_max3_f32 v14, v14, v53, v104
	v_max3_f32 v15, v15, v106, v107
	v_max3_f32 v14, v14, v105, v56
	v_max3_f32 v15, v15, v58, v59
	v_max3_f32 v14, v14, v57, v108
	v_max3_f32 v15, v15, v110, v111
	v_max3_f32 v14, v14, v109, v60
	v_max3_f32 v15, v15, v62, v63
	v_max3_f32 v14, v14, v61, v15
	v_mov_b32_e32 v15, v14
	s_nop 1
	v_permlane32_swap_b32_e32 v14, v15
	v_max_f32_e32 v14, v14, v15
	v_cmp_lt_f32_e32 vcc, s22, v14
	s_cmp_lg_u64 vcc, 0
	v_add_f32_e32 v0, v229, v0
	s_cselect_b64 s[4:5], -1, 0
	s_cbranch_vccnz .LBB0_776

.LBB0_1176:
	v_add_u32_e32 v203, s28, v200
	ds_read_b64_tr_b16 v[178:179], v203 offset:24576
	ds_read_b64_tr_b16 v[180:181], v203 offset:25088
	s_waitcnt lgkmcnt(9)
	v_mfma_f32_32x32x16_bf16 v[98:113], v[174:177], v[142:145], v[34:49]
	v_add_f32_e32 v82, v66, v67
	v_add_f32_e32 v82, v68, v82
	v_add_f32_e32 v82, v69, v82
	v_add_f32_e32 v82, v70, v82
	v_add_f32_e32 v82, v71, v82
	v_cvt_pk_bf16_f32 v130, v66, v67
	v_cvt_pk_bf16_f32 v131, v68, v69
	ds_read_b64_tr_b16 v[174:175], v203 offset:28672
	ds_read_b64_tr_b16 v[176:177], v203 offset:29184
	v_add_f32_e32 v66, v72, v82
	s_waitcnt lgkmcnt(10)
	v_mfma_f32_32x32x16_bf16 v[82:97], v[170:173], v[142:145], v[34:49]
	v_add_f32_e32 v66, v73, v66
	v_add_f32_e32 v66, v74, v66
	v_add_f32_e32 v114, v75, v66
	v_cvt_pk_bf16_f32 v132, v70, v71
	v_cvt_pk_bf16_f32 v133, v72, v73
	ds_read_b64_tr_b16 v[66:67], v203 offset:25600
	ds_read_b64_tr_b16 v[68:69], v203 offset:26112
	s_waitcnt lgkmcnt(11)
	v_mfma_f32_32x32x16_bf16 v[98:113], v[166:169], v[138:141], v[98:113]
	v_add_f32_e32 v70, v76, v114
	v_add_f32_e32 v70, v77, v70
	v_add_f32_e32 v70, v78, v70
	v_add_f32_e32 v114, v79, v70
	v_cvt_pk_bf16_f32 v122, v74, v75
	v_cvt_pk_bf16_f32 v123, v76, v77
	ds_read_b64_tr_b16 v[70:71], v203 offset:29696
	ds_read_b64_tr_b16 v[72:73], v203 offset:30208
	s_waitcnt lgkmcnt(12)
	v_mfma_f32_32x32x16_bf16 v[82:97], v[162:165], v[138:141], v[82:97]
	v_add_f32_e32 v74, v80, v114
	v_add_f32_e32 v74, v81, v74
	v_add_f32_e32 v74, v50, v74
	v_add_f32_e32 v114, v51, v74
	v_cvt_pk_bf16_f32 v124, v78, v79
	v_cvt_pk_bf16_f32 v125, v80, v81
	ds_read_b64_tr_b16 v[74:75], v203 offset:26624
	ds_read_b64_tr_b16 v[76:77], v203 offset:27136
	s_waitcnt lgkmcnt(13)
	v_mfma_f32_32x32x16_bf16 v[98:113], v[158:161], v[134:137], v[98:113]
	v_add_f32_e32 v78, v52, v114
	v_add_f32_e32 v78, v53, v78
	v_add_f32_e32 v78, v54, v78
	v_add_f32_e32 v78, v55, v78
	v_cvt_pk_bf16_f32 v118, v50, v51
	v_cvt_pk_bf16_f32 v119, v52, v53
	ds_read_b64_tr_b16 v[50:51], v203 offset:30720
	ds_read_b64_tr_b16 v[52:53], v203 offset:31232
	s_waitcnt lgkmcnt(14)
	v_mfma_f32_32x32x16_bf16 v[82:97], v[154:157], v[134:137], v[82:97]
	v_add_f32_e32 v78, v56, v78
	v_add_f32_e32 v78, v57, v78
	v_add_f32_e32 v78, v58, v78
	v_add_f32_e32 v78, v59, v78
	v_cvt_pk_bf16_f32 v120, v54, v55
	v_cvt_pk_bf16_f32 v121, v56, v57
	ds_read_b64_tr_b16 v[54:55], v203 offset:27648
	ds_read_b64_tr_b16 v[56:57], v203 offset:28160
	s_waitcnt lgkmcnt(14)
	v_mfma_f32_32x32x16_bf16 v[98:113], v[150:153], v[126:129], v[98:113]
	v_add_f32_e32 v78, v60, v78
	v_add_f32_e32 v78, v61, v78
	v_add_f32_e32 v78, v62, v78
	v_add_f32_e32 v78, v63, v78
	v_cvt_pk_bf16_f32 v114, v58, v59
	v_cvt_pk_bf16_f32 v115, v60, v61
	ds_read_b64_tr_b16 v[58:59], v203 offset:31744
	ds_read_b64_tr_b16 v[60:61], v203 offset:32256
	v_mfma_f32_32x32x16_bf16 v[82:97], v[146:149], v[126:129], v[82:97]
	v_add_f32_e32 v78, v64, v78
	v_add_f32_e32 v78, v65, v78
	v_cvt_pk_bf16_f32 v116, v62, v63
	v_cvt_pk_bf16_f32 v117, v64, v65
	s_movk_i32 s30, 0xc000
	s_mov_b32 s31, -1
	v_lshl_add_u64 v[62:63], v[188:189], 0, s[30:31]
	s_add_i32 s27, s26, s55
	s_mov_b32 s28, m0
	s_mov_b32 m0, s27
	s_nop 0
	global_load_lds_dwordx4 v[62:63], off
	s_mov_b32 m0, s28
	v_lshl_add_u64 v[62:63], v[186:187], 0, s[30:31]
	s_add_i32 s27, s23, s56
	s_mov_b32 s28, m0
	s_mov_b32 m0, s27
	s_nop 0
	global_load_lds_dwordx4 v[62:63], off
	s_mov_b32 m0, s28
	v_max_f32_e32 v62, v98, v99
	v_max3_f32 v63, v100, v101, v83
	v_max3_f32 v62, v62, v82, v84
	v_max3_f32 v62, v62, v85, v102
	v_max3_f32 v63, v63, v104, v105
	v_max3_f32 v62, v62, v103, v86
	v_max3_f32 v63, v63, v88, v89
	v_max3_f32 v62, v62, v87, v106
	v_max3_f32 v63, v63, v108, v109
	v_max3_f32 v62, v62, v107, v90
	v_max3_f32 v63, v63, v92, v93
	v_max3_f32 v62, v62, v91, v110
	v_max3_f32 v63, v63, v112, v113
	v_max3_f32 v62, v62, v111, v94
	v_max3_f32 v63, v63, v96, v97
	v_max3_f32 v62, v62, v95, v63
	v_mov_b32_e32 v63, v62
	s_nop 1
	v_permlane32_swap_b32_e32 v62, v63
	v_max_f32_e32 v62, v62, v63
	v_cmp_lt_f32_e32 vcc, s22, v62
	s_cmp_lg_u64 vcc, 0
	v_add_f32_e32 v202, v202, v78
	s_cselect_b64 s[28:29], -1, 0
	s_cbranch_vccnz .LBB0_1184

.LBB0_1179:
	s_add_i32 s27, s23, 0x2000
	s_cmpk_lg_i32 s23, 0x4000
	s_cselect_b32 s27, s27, 0
	v_add_u32_e32 v203, s26, v200
	ds_read_b64_tr_b16 v[150:151], v203 offset:24576
	ds_read_b64_tr_b16 v[152:153], v203 offset:25088
	s_waitcnt lgkmcnt(9)
	v_mfma_f32_32x32x16_bf16 v[66:81], v[62:65], v[142:145], v[34:49]
	v_add_f32_e32 v50, v98, v99
	v_add_f32_e32 v50, v100, v50
	v_add_f32_e32 v50, v101, v50
	v_add_f32_e32 v50, v102, v50
	v_add_f32_e32 v50, v103, v50
	v_cvt_pk_bf16_f32 v130, v98, v99
	v_cvt_pk_bf16_f32 v131, v100, v101
	ds_read_b64_tr_b16 v[146:147], v203 offset:28672
	ds_read_b64_tr_b16 v[148:149], v203 offset:29184
	v_add_f32_e32 v50, v104, v50
	v_add_f32_e32 v50, v105, v50
	v_add_f32_e32 v50, v106, v50
	v_add_f32_e32 v114, v107, v50
	s_waitcnt lgkmcnt(10)
	v_mfma_f32_32x32x16_bf16 v[50:65], v[174:177], v[142:145], v[34:49]
	v_cvt_pk_bf16_f32 v132, v102, v103
	v_cvt_pk_bf16_f32 v133, v104, v105
	ds_read_b64_tr_b16 v[98:99], v203 offset:25600
	ds_read_b64_tr_b16 v[100:101], v203 offset:26112
	s_waitcnt lgkmcnt(11)
	v_mfma_f32_32x32x16_bf16 v[66:81], v[178:181], v[138:141], v[66:81]
	v_add_f32_e32 v102, v108, v114
	v_add_f32_e32 v102, v109, v102
	v_add_f32_e32 v102, v110, v102
	v_add_f32_e32 v114, v111, v102
	v_cvt_pk_bf16_f32 v122, v106, v107
	v_cvt_pk_bf16_f32 v123, v108, v109
	ds_read_b64_tr_b16 v[102:103], v203 offset:29696
	ds_read_b64_tr_b16 v[104:105], v203 offset:30208
	s_waitcnt lgkmcnt(12)
	v_mfma_f32_32x32x16_bf16 v[50:65], v[170:173], v[138:141], v[50:65]
	v_add_f32_e32 v106, v112, v114
	v_add_f32_e32 v106, v113, v106
	v_add_f32_e32 v106, v82, v106
	v_add_f32_e32 v114, v83, v106
	v_cvt_pk_bf16_f32 v124, v110, v111
	v_cvt_pk_bf16_f32 v125, v112, v113
	ds_read_b64_tr_b16 v[106:107], v203 offset:26624
	ds_read_b64_tr_b16 v[108:109], v203 offset:27136
	s_waitcnt lgkmcnt(13)
	v_mfma_f32_32x32x16_bf16 v[66:81], v[166:169], v[134:137], v[66:81]
	v_add_f32_e32 v110, v84, v114
	v_add_f32_e32 v110, v85, v110
	v_add_f32_e32 v110, v86, v110
	v_add_f32_e32 v110, v87, v110
	v_cvt_pk_bf16_f32 v118, v82, v83
	v_cvt_pk_bf16_f32 v119, v84, v85
	ds_read_b64_tr_b16 v[82:83], v203 offset:30720
	ds_read_b64_tr_b16 v[84:85], v203 offset:31232
	s_waitcnt lgkmcnt(14)
	v_mfma_f32_32x32x16_bf16 v[50:65], v[162:165], v[134:137], v[50:65]
	v_add_f32_e32 v110, v88, v110
	v_add_f32_e32 v110, v89, v110
	v_add_f32_e32 v110, v90, v110
	v_add_f32_e32 v110, v91, v110
	v_cvt_pk_bf16_f32 v120, v86, v87
	v_cvt_pk_bf16_f32 v121, v88, v89
	ds_read_b64_tr_b16 v[86:87], v203 offset:27648
	ds_read_b64_tr_b16 v[88:89], v203 offset:28160
	s_waitcnt lgkmcnt(14)
	v_mfma_f32_32x32x16_bf16 v[66:81], v[158:161], v[126:129], v[66:81]
	v_add_f32_e32 v110, v92, v110
	v_add_f32_e32 v110, v93, v110
	v_add_f32_e32 v110, v94, v110
	v_add_f32_e32 v110, v95, v110
	v_cvt_pk_bf16_f32 v114, v90, v91
	v_cvt_pk_bf16_f32 v115, v92, v93
	ds_read_b64_tr_b16 v[90:91], v203 offset:31744
	ds_read_b64_tr_b16 v[92:93], v203 offset:32256
	v_mfma_f32_32x32x16_bf16 v[50:65], v[154:157], v[126:129], v[50:65]
	v_add_f32_e32 v110, v96, v110
	v_add_f32_e32 v110, v97, v110
	v_cvt_pk_bf16_f32 v116, v94, v95
	v_cvt_pk_bf16_f32 v117, v96, v97
	v_max_f32_e32 v94, v66, v67
	s_nop 3
	s_nop 2
	v_max3_f32 v95, v68, v69, v51
	v_max3_f32 v94, v94, v50, v52
	v_max3_f32 v94, v94, v53, v70
	v_max3_f32 v95, v95, v72, v73
	v_max3_f32 v94, v94, v71, v54
	v_max3_f32 v95, v95, v56, v57
	v_max3_f32 v94, v94, v55, v74
	v_max3_f32 v95, v95, v76, v77
	v_max3_f32 v94, v94, v75, v58
	v_max3_f32 v95, v95, v60, v61
	v_max3_f32 v94, v94, v59, v78
	v_max3_f32 v95, v95, v80, v81
	v_max3_f32 v94, v94, v79, v62
	v_max3_f32 v95, v95, v64, v65
	v_max3_f32 v94, v94, v63, v95
	v_mov_b32_e32 v95, v94
	s_nop 1
	v_permlane32_swap_b32_e32 v94, v95
	v_max_f32_e32 v95, v95, v95
	v_max_f32_e32 v94, v94, v94
	s_add_i32 s26, s23, s55
	s_mov_b32 s28, m0
	s_mov_b32 m0, s26
	s_nop 0
	global_load_lds_dwordx4 v[188:189], off
	s_mov_b32 m0, s28
	v_max_f32_e32 v94, v94, v95
	s_add_i32 s26, s27, s56
	s_mov_b32 s28, m0
	s_mov_b32 m0, s26
	s_nop 0
	global_load_lds_dwordx4 v[186:187], off
	s_mov_b32 m0, s28
	v_cmp_lt_f32_e32 vcc, s22, v94
	s_cmp_lg_u64 vcc, 0
	v_add_f32_e32 v202, v202, v110
	s_cselect_b64 s[28:29], -1, 0
	s_cbranch_vccnz .LBB0_1187

.LBB0_1192:
	v_add_u32_e32 v0, s10, v200
	ds_read_b64_tr_b16 v[178:179], v0 offset:24576
	ds_read_b64_tr_b16 v[180:181], v0 offset:25088
	s_waitcnt lgkmcnt(9)
	v_mfma_f32_32x32x16_bf16 v[98:113], v[174:177], v[142:145], v[34:49]
	v_add_f32_e32 v82, v66, v67
	v_add_f32_e32 v82, v68, v82
	v_add_f32_e32 v82, v69, v82
	v_add_f32_e32 v82, v70, v82
	v_add_f32_e32 v82, v71, v82
	v_cvt_pk_bf16_f32 v130, v66, v67
	v_cvt_pk_bf16_f32 v131, v68, v69
	ds_read_b64_tr_b16 v[174:175], v0 offset:28672
	ds_read_b64_tr_b16 v[176:177], v0 offset:29184
	v_add_f32_e32 v66, v72, v82
	s_waitcnt lgkmcnt(10)
	v_mfma_f32_32x32x16_bf16 v[82:97], v[170:173], v[142:145], v[34:49]
	v_add_f32_e32 v66, v73, v66
	v_add_f32_e32 v66, v74, v66
	v_add_f32_e32 v114, v75, v66
	v_cvt_pk_bf16_f32 v132, v70, v71
	v_cvt_pk_bf16_f32 v133, v72, v73
	ds_read_b64_tr_b16 v[66:67], v0 offset:25600
	ds_read_b64_tr_b16 v[68:69], v0 offset:26112
	s_waitcnt lgkmcnt(11)
	v_mfma_f32_32x32x16_bf16 v[98:113], v[166:169], v[138:141], v[98:113]
	v_add_f32_e32 v70, v76, v114
	v_add_f32_e32 v70, v77, v70
	v_add_f32_e32 v70, v78, v70
	v_add_f32_e32 v114, v79, v70
	v_cvt_pk_bf16_f32 v122, v74, v75
	v_cvt_pk_bf16_f32 v123, v76, v77
	ds_read_b64_tr_b16 v[70:71], v0 offset:29696
	ds_read_b64_tr_b16 v[72:73], v0 offset:30208
	s_waitcnt lgkmcnt(12)
	v_mfma_f32_32x32x16_bf16 v[82:97], v[162:165], v[138:141], v[82:97]
	v_add_f32_e32 v74, v80, v114
	v_add_f32_e32 v74, v81, v74
	v_add_f32_e32 v74, v50, v74
	v_add_f32_e32 v114, v51, v74
	v_cvt_pk_bf16_f32 v124, v78, v79
	v_cvt_pk_bf16_f32 v125, v80, v81
	ds_read_b64_tr_b16 v[74:75], v0 offset:26624
	ds_read_b64_tr_b16 v[76:77], v0 offset:27136
	s_waitcnt lgkmcnt(13)
	v_mfma_f32_32x32x16_bf16 v[98:113], v[158:161], v[134:137], v[98:113]
	v_add_f32_e32 v78, v52, v114
	v_add_f32_e32 v78, v53, v78
	v_add_f32_e32 v78, v54, v78
	v_add_f32_e32 v78, v55, v78
	v_cvt_pk_bf16_f32 v118, v50, v51
	v_cvt_pk_bf16_f32 v119, v52, v53
	ds_read_b64_tr_b16 v[50:51], v0 offset:30720
	ds_read_b64_tr_b16 v[52:53], v0 offset:31232
	s_waitcnt lgkmcnt(14)
	v_mfma_f32_32x32x16_bf16 v[82:97], v[154:157], v[134:137], v[82:97]
	v_add_f32_e32 v78, v56, v78
	v_add_f32_e32 v78, v57, v78
	v_add_f32_e32 v78, v58, v78
	v_add_f32_e32 v78, v59, v78
	v_cvt_pk_bf16_f32 v120, v54, v55
	v_cvt_pk_bf16_f32 v121, v56, v57
	ds_read_b64_tr_b16 v[54:55], v0 offset:27648
	ds_read_b64_tr_b16 v[56:57], v0 offset:28160
	s_waitcnt lgkmcnt(14)
	v_mfma_f32_32x32x16_bf16 v[98:113], v[150:153], v[126:129], v[98:113]
	v_add_f32_e32 v78, v60, v78
	v_add_f32_e32 v78, v61, v78
	v_add_f32_e32 v78, v62, v78
	v_add_f32_e32 v78, v63, v78
	v_cvt_pk_bf16_f32 v114, v58, v59
	v_cvt_pk_bf16_f32 v115, v60, v61
	ds_read_b64_tr_b16 v[58:59], v0 offset:31744
	ds_read_b64_tr_b16 v[60:61], v0 offset:32256
	v_mfma_f32_32x32x16_bf16 v[82:97], v[146:149], v[126:129], v[82:97]
	v_add_f32_e32 v0, v64, v78
	v_add_f32_e32 v0, v65, v0
	v_cvt_pk_bf16_f32 v116, v62, v63
	v_cvt_pk_bf16_f32 v117, v64, v65
	s_cmp_gt_u32 s13, 64
	s_cselect_b64 s[10:11], -1, 0
	s_and_b64 vcc, exec, s[10:11]
	s_cbranch_vccnz .LBB0_1194
	v_lshl_add_u64 v[62:63], v[184:185], 0, s[8:9]
	s_add_i32 s27, s26, s55
	s_mov_b32 s28, m0
	s_mov_b32 m0, s27
	s_nop 0
	global_load_lds_dwordx4 v[62:63], off
	s_mov_b32 m0, s28
.LBB0_1194:
	v_lshl_add_u64 v[188:189], v[182:183], 0, s[8:9]
	s_mov_b64 s[28:29], 0x100000
	v_lshl_add_u64 v[62:63], v[188:189], 0, s[28:29]
	s_add_i32 s27, s23, s56
	s_mov_b32 s28, m0
	s_mov_b32 m0, s27
	s_nop 0
	global_load_lds_dwordx4 v[62:63], off
	s_mov_b32 m0, s28
	v_max_f32_e32 v62, v98, v99
	v_max3_f32 v63, v100, v101, v83
	v_max3_f32 v62, v62, v82, v84
	v_max3_f32 v62, v62, v85, v102
	v_max3_f32 v63, v63, v104, v105
	v_max3_f32 v62, v62, v103, v86
	v_max3_f32 v63, v63, v88, v89
	v_max3_f32 v62, v62, v87, v106
	v_max3_f32 v63, v63, v108, v109
	v_max3_f32 v62, v62, v107, v90
	v_max3_f32 v63, v63, v92, v93
	v_max3_f32 v62, v62, v91, v110
	v_max3_f32 v63, v63, v112, v113
	v_max3_f32 v62, v62, v111, v94
	v_max3_f32 v63, v63, v96, v97
	v_max3_f32 v62, v62, v95, v63
	v_mov_b32_e32 v63, v62
	s_nop 1
	v_permlane32_swap_b32_e32 v62, v63
	v_max_f32_e32 v62, v62, v63
	v_cmp_lt_f32_e32 vcc, s22, v62
	s_cmp_lg_u64 vcc, 0
	v_add_f32_e32 v0, v202, v0
	s_cselect_b64 s[28:29], -1, 0
	s_cbranch_vccnz .LBB0_1220

.LBB0_1203:
	v_add_u32_e32 v202, s26, v200
	ds_read_b64_tr_b16 v[154:155], v202 offset:24576
	ds_read_b64_tr_b16 v[156:157], v202 offset:25088
	s_waitcnt lgkmcnt(9)
	v_mfma_f32_32x32x16_bf16 v[66:81], v[62:65], v[142:145], v[34:49]
	v_add_f32_e32 v50, v98, v99
	v_add_f32_e32 v50, v100, v50
	v_add_f32_e32 v50, v101, v50
	v_add_f32_e32 v50, v102, v50
	v_add_f32_e32 v50, v103, v50
	v_cvt_pk_bf16_f32 v130, v98, v99
	v_cvt_pk_bf16_f32 v131, v100, v101
	ds_read_b64_tr_b16 v[150:151], v202 offset:28672
	ds_read_b64_tr_b16 v[152:153], v202 offset:29184
	v_add_f32_e32 v50, v104, v50
	v_add_f32_e32 v50, v105, v50
	v_add_f32_e32 v50, v106, v50
	v_add_f32_e32 v114, v107, v50
	s_waitcnt lgkmcnt(10)
	v_mfma_f32_32x32x16_bf16 v[50:65], v[174:177], v[142:145], v[34:49]
	v_cvt_pk_bf16_f32 v132, v102, v103
	v_cvt_pk_bf16_f32 v133, v104, v105
	ds_read_b64_tr_b16 v[98:99], v202 offset:25600
	ds_read_b64_tr_b16 v[100:101], v202 offset:26112
	s_waitcnt lgkmcnt(11)
	v_mfma_f32_32x32x16_bf16 v[66:81], v[178:181], v[138:141], v[66:81]
	v_add_f32_e32 v102, v108, v114
	v_add_f32_e32 v102, v109, v102
	v_add_f32_e32 v102, v110, v102
	v_add_f32_e32 v114, v111, v102
	v_cvt_pk_bf16_f32 v122, v106, v107
	v_cvt_pk_bf16_f32 v123, v108, v109
	ds_read_b64_tr_b16 v[102:103], v202 offset:29696
	ds_read_b64_tr_b16 v[104:105], v202 offset:30208
	s_waitcnt lgkmcnt(12)
	v_mfma_f32_32x32x16_bf16 v[50:65], v[170:173], v[138:141], v[50:65]
	v_add_f32_e32 v106, v112, v114
	v_add_f32_e32 v106, v113, v106
	v_add_f32_e32 v106, v82, v106
	v_add_f32_e32 v114, v83, v106
	v_cvt_pk_bf16_f32 v124, v110, v111
	v_cvt_pk_bf16_f32 v125, v112, v113
	ds_read_b64_tr_b16 v[106:107], v202 offset:26624
	ds_read_b64_tr_b16 v[108:109], v202 offset:27136
	s_waitcnt lgkmcnt(13)
	v_mfma_f32_32x32x16_bf16 v[66:81], v[166:169], v[134:137], v[66:81]
	v_add_f32_e32 v110, v84, v114
	v_add_f32_e32 v110, v85, v110
	v_add_f32_e32 v110, v86, v110
	v_add_f32_e32 v110, v87, v110
	v_cvt_pk_bf16_f32 v118, v82, v83
	v_cvt_pk_bf16_f32 v119, v84, v85
	ds_read_b64_tr_b16 v[82:83], v202 offset:30720
	ds_read_b64_tr_b16 v[84:85], v202 offset:31232
	s_waitcnt lgkmcnt(14)
	v_mfma_f32_32x32x16_bf16 v[50:65], v[162:165], v[134:137], v[50:65]
	v_add_f32_e32 v110, v88, v110
	v_add_f32_e32 v110, v89, v110
	v_add_f32_e32 v110, v90, v110
	v_add_f32_e32 v110, v91, v110
	v_cvt_pk_bf16_f32 v120, v86, v87
	v_cvt_pk_bf16_f32 v121, v88, v89
	ds_read_b64_tr_b16 v[86:87], v202 offset:27648
	ds_read_b64_tr_b16 v[88:89], v202 offset:28160
	s_waitcnt lgkmcnt(14)
	v_mfma_f32_32x32x16_bf16 v[66:81], v[158:161], v[126:129], v[66:81]
	v_add_f32_e32 v110, v92, v110
	v_add_f32_e32 v110, v93, v110
	v_add_f32_e32 v110, v94, v110
	v_add_f32_e32 v110, v95, v110
	v_cvt_pk_bf16_f32 v114, v90, v91
	v_cvt_pk_bf16_f32 v115, v92, v93
	ds_read_b64_tr_b16 v[90:91], v202 offset:31744
	ds_read_b64_tr_b16 v[92:93], v202 offset:32256
	v_mfma_f32_32x32x16_bf16 v[50:65], v[146:149], v[126:129], v[50:65]
	v_add_f32_e32 v110, v96, v110
	v_add_f32_e32 v110, v97, v110
	v_cvt_pk_bf16_f32 v116, v94, v95
	v_cvt_pk_bf16_f32 v117, v96, v97
	s_cmp_gt_u32 s13, 63
	s_cselect_b64 s[28:29], -1, 0
	s_and_b64 vcc, exec, s[28:29]
	s_cbranch_vccnz .LBB0_1205
	v_lshl_add_u64 v[94:95], v[186:187], 0, s[8:9]
	s_mov_b64 s[26:27], 0x10000
	v_lshl_add_u64 v[94:95], v[94:95], 0, s[26:27]
	s_add_i32 s26, s23, s55
	s_mov_b32 s27, m0
	s_mov_b32 m0, s26
	s_nop 0
	global_load_lds_dwordx4 v[94:95], off
	s_mov_b32 m0, s27
.LBB0_1205:
	s_add_i32 s26, s23, 0x2000
	s_cmpk_lg_i32 s23, 0x4000
	s_mov_b64 s[30:31], 0x104000
	s_cselect_b32 s26, s26, 0
	v_lshl_add_u64 v[94:95], v[188:189], 0, s[30:31]
	v_add_f32_e32 v202, v0, v110
	s_add_i32 s27, s26, s56
	s_mov_b32 s30, m0
	s_mov_b32 m0, s27
	s_nop 0
	global_load_lds_dwordx4 v[94:95], off
	s_mov_b32 m0, s30
	v_max_f32_e32 v0, v66, v67
	v_max3_f32 v94, v68, v69, v51
	v_max3_f32 v0, v0, v50, v52
	v_max3_f32 v0, v0, v53, v70
	v_max3_f32 v94, v94, v72, v73
	v_max3_f32 v0, v0, v71, v54
	v_max3_f32 v94, v94, v56, v57
	v_max3_f32 v0, v0, v55, v74
	v_max3_f32 v94, v94, v76, v77
	v_max3_f32 v0, v0, v75, v58
	v_max3_f32 v94, v94, v60, v61
	v_max3_f32 v0, v0, v59, v78
	v_max3_f32 v94, v94, v80, v81
	v_max3_f32 v0, v0, v79, v62
	v_max3_f32 v94, v94, v64, v65
	v_max3_f32 v0, v0, v63, v94
	v_mov_b32_e32 v94, v0
	s_nop 1
	v_permlane32_swap_b32_e32 v0, v94
	v_max_f32_e32 v0, v0, v94
	v_cmp_lt_f32_e32 vcc, s22, v0
	s_cmp_lg_u64 vcc, 0
	s_cselect_b64 s[30:31], -1, 0
	s_cbranch_vccnz .LBB0_1223

.LBB0_1226:
	ds_read_b64_tr_b16 v[98:99], v200 offset:24576
	ds_read_b64_tr_b16 v[100:101], v200 offset:25088
	s_waitcnt lgkmcnt(9)
	v_mfma_f32_32x32x16_bf16 v[82:97], v[174:177], v[142:145], v[34:49]
	v_add_f32_e32 v0, v66, v67
	v_add_f32_e32 v0, v68, v0
	v_add_f32_e32 v0, v69, v0
	v_add_f32_e32 v0, v70, v0
	v_add_f32_e32 v0, v71, v0
	v_cvt_pk_bf16_f32 v130, v66, v67
	v_cvt_pk_bf16_f32 v131, v68, v69
	ds_read_b64_tr_b16 v[66:67], v200 offset:28672
	ds_read_b64_tr_b16 v[68:69], v200 offset:29184
	s_waitcnt lgkmcnt(10)
	v_mfma_f32_32x32x16_bf16 v[34:49], v[170:173], v[142:145], v[34:49]
	v_add_f32_e32 v0, v72, v0
	v_add_f32_e32 v0, v73, v0
	v_add_f32_e32 v0, v74, v0
	v_add_f32_e32 v0, v75, v0
	v_cvt_pk_bf16_f32 v132, v70, v71
	v_cvt_pk_bf16_f32 v133, v72, v73
	ds_read_b64_tr_b16 v[70:71], v200 offset:25600
	ds_read_b64_tr_b16 v[72:73], v200 offset:26112
	s_waitcnt lgkmcnt(11)
	v_mfma_f32_32x32x16_bf16 v[82:97], v[166:169], v[138:141], v[82:97]
	v_add_f32_e32 v0, v76, v0
	v_add_f32_e32 v0, v77, v0
	v_add_f32_e32 v0, v78, v0
	v_add_f32_e32 v0, v79, v0
	v_cvt_pk_bf16_f32 v122, v74, v75
	v_cvt_pk_bf16_f32 v123, v76, v77
	ds_read_b64_tr_b16 v[74:75], v200 offset:29696
	ds_read_b64_tr_b16 v[76:77], v200 offset:30208
	s_waitcnt lgkmcnt(12)
	v_mfma_f32_32x32x16_bf16 v[34:49], v[162:165], v[138:141], v[34:49]
	v_add_f32_e32 v0, v80, v0
	v_add_f32_e32 v0, v81, v0
	v_add_f32_e32 v0, v50, v0
	v_add_f32_e32 v0, v51, v0
	v_cvt_pk_bf16_f32 v124, v78, v79
	v_cvt_pk_bf16_f32 v125, v80, v81
	ds_read_b64_tr_b16 v[78:79], v200 offset:26624
	ds_read_b64_tr_b16 v[80:81], v200 offset:27136
	s_waitcnt lgkmcnt(13)
	v_mfma_f32_32x32x16_bf16 v[82:97], v[158:161], v[134:137], v[82:97]
	v_add_f32_e32 v0, v52, v0
	v_add_f32_e32 v0, v53, v0
	v_add_f32_e32 v0, v54, v0
	v_add_f32_e32 v0, v55, v0
	v_cvt_pk_bf16_f32 v118, v50, v51
	v_cvt_pk_bf16_f32 v119, v52, v53
	ds_read_b64_tr_b16 v[102:103], v200 offset:30720
	ds_read_b64_tr_b16 v[104:105], v200 offset:31232
	s_waitcnt lgkmcnt(14)
	v_mfma_f32_32x32x16_bf16 v[34:49], v[154:157], v[134:137], v[34:49]
	v_add_f32_e32 v0, v56, v0
	v_add_f32_e32 v0, v57, v0
	v_add_f32_e32 v0, v58, v0
	v_add_f32_e32 v0, v59, v0
	v_cvt_pk_bf16_f32 v120, v54, v55
	v_cvt_pk_bf16_f32 v121, v56, v57
	ds_read_b64_tr_b16 v[106:107], v200 offset:27648
	ds_read_b64_tr_b16 v[108:109], v200 offset:28160
	s_waitcnt lgkmcnt(14)
	v_mfma_f32_32x32x16_bf16 v[82:97], v[150:153], v[126:129], v[82:97]
	v_add_f32_e32 v0, v60, v0
	v_add_f32_e32 v0, v61, v0
	v_add_f32_e32 v0, v62, v0
	v_add_f32_e32 v0, v63, v0
	v_cvt_pk_bf16_f32 v114, v58, v59
	v_cvt_pk_bf16_f32 v115, v60, v61
	ds_read_b64_tr_b16 v[110:111], v200 offset:31744
	ds_read_b64_tr_b16 v[112:113], v200 offset:32256
	v_mfma_f32_32x32x16_bf16 v[34:49], v[146:149], v[126:129], v[34:49]
	v_add_f32_e32 v0, v64, v0
	v_add_f32_e32 v0, v65, v0
	v_cvt_pk_bf16_f32 v116, v62, v63
	v_cvt_pk_bf16_f32 v117, v64, v65
	v_max_f32_e32 v50, v82, v83
	s_nop 3
	s_nop 2
	v_max3_f32 v51, v84, v85, v35
	v_max3_f32 v50, v50, v34, v36
	v_max3_f32 v50, v50, v37, v86
	v_max3_f32 v51, v51, v88, v89
	v_max3_f32 v50, v50, v87, v38
	v_max3_f32 v51, v51, v40, v41
	v_max3_f32 v50, v50, v39, v90
	v_max3_f32 v51, v51, v92, v93
	v_max3_f32 v50, v50, v91, v42
	v_max3_f32 v51, v51, v44, v45
	v_max3_f32 v50, v50, v43, v94
	v_max3_f32 v51, v51, v96, v97
	v_max3_f32 v50, v50, v95, v46
	v_max3_f32 v51, v51, v48, v49
	v_max3_f32 v50, v50, v47, v51
	v_mov_b32_e32 v51, v50
	s_nop 1
	v_permlane32_swap_b32_e32 v50, v51
	v_max_f32_e32 v50, v50, v51
	v_cmp_lt_f32_e32 vcc, s22, v50
	s_cmp_lg_u64 vcc, 0
	v_add_f32_e32 v0, v202, v0
	s_cselect_b64 s[8:9], -1, 0
	s_cbranch_vccnz .LBB0_1258

.LBB0_1265:
	v_readlane_b32 s1, v252, 42
	s_lshl_b32 s12, s1, 1
	s_add_u32 s4, s9, s12
	v_and_b32_e32 v184, 63, v36
	s_addc_u32 s5, s11, 0
	s_lshl_b32 s10, s8, 5
	s_mul_i32 s1, s8, 0x6c000
	v_mul_u32_u24_e32 v0, 0x1b00, v184
	s_mul_hi_i32 s7, s10, 0x3600
	s_add_u32 s6, s4, s1
	v_lshlrev_b32_e32 v0, 1, v0
	s_addc_u32 s7, s5, s7
	v_lshl_add_u64 v[4:5], s[4:5], 0, v[0:1]
	s_lshl_b32 s1, s8, 4
	v_bfe_u32 v0, v36, 2, 4
	v_and_or_b32 v0, s1, 48, v0
	s_and_b32 s23, s0, 0x3fffffc0
	v_mul_u32_u24_e32 v0, 0x1b00, v0
	s_ashr_i32 s0, s0, 3
	v_lshlrev_b32_e32 v0, 1, v0
	s_andn2_b32 s0, s0, 31
	v_lshlrev_b32_e32 v185, 3, v2
	v_lshl_add_u64 v[6:7], s[4:5], 0, v[0:1]
	s_ashr_i32 s1, s0, 31
	v_and_b32_e32 v188, 24, v185
	v_lshl_add_u64 v[6:7], s[0:1], 1, v[6:7]
	v_lshlrev_b32_e32 v0, 1, v188
	s_lshl_b32 s26, s8, 3
	v_lshl_add_u64 v[38:39], v[6:7], 0, v[0:1]
	s_mov_b64 s[0:1], 0x1400
	s_ashr_i32 s27, s26, 31
	v_lshl_add_u64 v[182:183], v[38:39], 0, s[0:1]
	s_lshl_b32 s0, s8, 10
	s_cmp_lg_u32 0, -1
	v_lshl_add_u64 v[34:35], s[26:27], 1, v[4:5]
	s_mov_b64 s[26:27], 0x1000
	s_cselect_b32 s1, 0, 0
	v_and_b32_e32 v186, 31, v36
	v_lshl_add_u64 v[4:5], v[34:35], 0, s[26:27]
	s_add_i32 s4, s1, s0
	s_mov_b32 s0, m0
	s_mov_b32 m0, s4
	s_nop 0
	global_load_lds_dwordx4 v[4:5], off
	s_mov_b32 m0, s0
	s_add_i32 s13, s4, 0x6000
	s_mov_b32 s0, m0
	s_mov_b32 m0, s13
	s_nop 0
	global_load_lds_dwordx4 v[182:183], off
	s_mov_b32 m0, s0
	v_mul_u32_u24_e32 v0, 0x1b00, v186
	v_bfe_u32 v187, v36, 5, 1
	s_mov_b64 s[0:1], 0xd9000
	v_lshlrev_b32_e32 v0, 1, v0
	v_lshl_add_u64 v[2:3], v[34:35], 0, s[0:1]
	s_add_i32 s0, s4, 0x2000
	s_mov_b32 s1, m0
	s_mov_b32 m0, s0
	s_nop 0
	global_load_lds_dwordx4 v[2:3], off
	s_mov_b32 m0, s1
	v_lshl_or_b32 v0, v187, 4, v0
	global_load_dwordx4 v[142:145], v0, s[6:7] offset:3072
	global_load_dwordx4 v[138:141], v0, s[6:7] offset:3104
	global_load_dwordx4 v[118:121], v0, s[6:7] offset:3136
	global_load_dwordx4 v[114:117], v0, s[6:7] offset:3168
	v_mov_b32_e32 v2, v1
	v_mov_b32_e32 v3, v1
	v_mov_b32_e32 v4, v1
	v_mov_b32_e32 v5, v1
	v_mov_b32_e32 v6, v1
	v_mov_b32_e32 v7, v1
	v_mov_b32_e32 v8, v1
	v_mov_b32_e32 v9, v1
	v_mov_b32_e32 v10, v1
	v_mov_b32_e32 v11, v1
	v_mov_b32_e32 v12, v1
	v_mov_b32_e32 v13, v1
	v_mov_b32_e32 v14, v1
	v_mov_b32_e32 v15, v1
	v_lshlrev_b32_e32 v0, 4, v186
	v_lshl_add_u32 v16, v187, 10, 0
	v_add_u32_e32 v194, v16, v0
	v_mov_b32_e32 v0, v1
	v_mov_b64_e32 v[16:17], v[14:15]
	s_mov_b64 s[0:1], 0x1b1000
	v_mov_b64_e32 v[14:15], v[12:13]
	v_mov_b64_e32 v[12:13], v[10:11]
	v_mov_b64_e32 v[10:11], v[8:9]
	v_mov_b64_e32 v[8:9], v[6:7]
	v_mov_b64_e32 v[6:7], v[4:5]
	v_mov_b64_e32 v[4:5], v[2:3]
	v_mov_b64_e32 v[2:3], v[0:1]
	v_lshl_add_u64 v[18:19], v[34:35], 0, s[0:1]
	s_add_i32 s0, s4, 0x4000
	s_mov_b32 s1, m0
	s_mov_b32 m0, s0
	s_nop 0
	global_load_lds_dwordx4 v[18:19], off
	s_mov_b32 m0, s1
	s_waitcnt vmcnt(3) lgkmcnt(0)
	s_barrier
	ds_read_b128 v[40:43], v194
	ds_read_b128 v[44:47], v194 offset:512
	v_lshlrev_b32_e32 v0, 1, v36
	v_lshlrev_b32_e32 v36, 4, v36
	v_and_b32_e32 v0, 32, v0
	v_and_b32_e32 v36, 0xc0, v36
	v_lshl_or_b32 v189, v187, 8, v36
	v_add3_u32 v36, 0, v0, v188
	v_add_u32_e32 v191, v36, v189
	s_lshl_b32 s0, s23, 2
	s_add_i32 s23, s0, 0
	s_mov_b64 s[0:1], 0x289000
	v_lshl_add_u32 v190, v186, 2, s23
	s_waitcnt vmcnt(3) lgkmcnt(1)
	v_mfma_f32_32x32x16_bf16 v[18:33], v[40:43], v[142:145], v[2:17]
	s_waitcnt lgkmcnt(0)
	v_mfma_f32_32x32x16_bf16 v[2:17], v[44:47], v[142:145], v[2:17]
	ds_read_b128 v[40:43], v194 offset:2048
	ds_read_b128 v[44:47], v194 offset:2560
	s_waitcnt vmcnt(2) lgkmcnt(1)
	v_mfma_f32_32x32x16_bf16 v[18:33], v[40:43], v[138:141], v[18:33]
	s_waitcnt lgkmcnt(0)
	v_mfma_f32_32x32x16_bf16 v[2:17], v[44:47], v[138:141], v[2:17]
	ds_read_b128 v[40:43], v194 offset:4096
	ds_read_b128 v[44:47], v194 offset:4608
	s_waitcnt vmcnt(1) lgkmcnt(1)
	v_mfma_f32_32x32x16_bf16 v[18:33], v[40:43], v[118:121], v[18:33]
	ds_read_b128 v[40:43], v194 offset:6144
	s_waitcnt lgkmcnt(1)
	v_mfma_f32_32x32x16_bf16 v[2:17], v[44:47], v[118:121], v[2:17]
	ds_read_b128 v[44:47], v194 offset:6656
	s_waitcnt vmcnt(0) lgkmcnt(1)
	v_mfma_f32_32x32x16_bf16 v[18:33], v[40:43], v[114:117], v[18:33]
	s_waitcnt lgkmcnt(0)
	v_mfma_f32_32x32x16_bf16 v[2:17], v[44:47], v[114:117], v[2:17]
	s_nop 15
	s_nop 7
	s_nop 0
	v_max3_f32 v36, v18, v19, v2
	v_max3_f32 v37, v20, v21, v3
	s_nop 0
	v_max3_f32 v36, v36, v4, v5
	v_max3_f32 v37, v37, v24, v25
	s_nop 0
	v_max3_f32 v36, v36, v22, v23
	v_max3_f32 v37, v37, v8, v9
	s_nop 0
	v_max3_f32 v36, v36, v6, v7
	v_max3_f32 v37, v37, v28, v29
	s_nop 0
	v_max3_f32 v36, v36, v26, v27
	v_max3_f32 v37, v37, v12, v13
	s_nop 0
	v_max3_f32 v36, v36, v10, v11
	v_max3_f32 v37, v37, v32, v33
	s_nop 0
	v_max3_f32 v36, v36, v30, v31
	v_max3_f32 v37, v37, v16, v17
	s_nop 0
	v_max3_f32 v36, v36, v14, v15
	s_nop 0
	v_max_f32_e32 v36, v36, v37
	s_nop 0
	v_mov_b32_e32 v37, v36
	s_nop 1
	v_permlane32_swap_b32_e32 v36, v37
	v_max_f32_e32 v36, v36, v37
	s_nop 0
	v_add_f32_e32 v192, v1, v36
	v_sub_f32_e32 v37, v2, v36
	v_sub_f32_e32 v18, v18, v36
	v_sub_f32_e32 v19, v19, v36
	v_sub_f32_e32 v40, v3, v36
	v_sub_f32_e32 v20, v20, v36
	s_nop 0
	v_xor_b32_e32 v2, 0x80000000, v192
	v_sub_f32_e32 v41, v4, v36
	v_sub_f32_e32 v21, v21, v36
	v_sub_f32_e32 v42, v5, v36
	v_sub_f32_e32 v22, v22, v36
	v_sub_f32_e32 v43, v6, v36
	v_sub_f32_e32 v23, v23, v36
	v_sub_f32_e32 v44, v7, v36
	v_sub_f32_e32 v24, v24, v36
	v_sub_f32_e32 v45, v8, v36
	v_sub_f32_e32 v25, v25, v36
	v_sub_f32_e32 v46, v9, v36
	v_sub_f32_e32 v26, v26, v36
	v_sub_f32_e32 v47, v10, v36
	v_sub_f32_e32 v27, v27, v36
	v_sub_f32_e32 v48, v11, v36
	v_sub_f32_e32 v28, v28, v36
	v_sub_f32_e32 v49, v12, v36
	v_sub_f32_e32 v29, v29, v36
	v_sub_f32_e32 v50, v13, v36
	v_sub_f32_e32 v30, v30, v36
	v_sub_f32_e32 v51, v14, v36
	v_sub_f32_e32 v31, v31, v36
	v_sub_f32_e32 v52, v15, v36
	v_sub_f32_e32 v32, v32, v36
	v_sub_f32_e32 v53, v16, v36
	v_sub_f32_e32 v33, v33, v36
	v_sub_f32_e32 v36, v17, v36
	v_mov_b32_e32 v3, v2
	v_mov_b32_e32 v4, v2
	v_mov_b32_e32 v5, v2
	v_mov_b32_e32 v6, v2
	v_mov_b32_e32 v7, v2
	v_mov_b32_e32 v8, v2
	v_mov_b32_e32 v9, v2
	v_mov_b32_e32 v10, v2
	v_mov_b32_e32 v11, v2
	v_mov_b32_e32 v12, v2
	v_mov_b32_e32 v13, v2
	v_mov_b32_e32 v14, v2
	v_mov_b32_e32 v15, v2
	v_mov_b32_e32 v16, v2
	v_mov_b32_e32 v17, v2
	s_waitcnt vmcnt(0) lgkmcnt(0)
	s_barrier
	v_exp_f32_e32 v54, v18
	v_exp_f32_e32 v55, v19
	v_lshl_add_u64 v[18:19], v[34:35], 0, s[0:1]
	s_mov_b32 s0, m0
	s_mov_b32 m0, s4
	s_nop 0
	global_load_lds_dwordx4 v[18:19], off
	s_mov_b32 m0, s0
	s_mov_b64 s[0:1], 0xd9400
	v_lshl_add_u64 v[18:19], v[38:39], 0, s[0:1]
	s_add_i32 s0, s4, 0x8000
	s_mov_b32 s1, m0
	s_mov_b32 m0, s0
	s_nop 0
	global_load_lds_dwordx4 v[18:19], off
	s_mov_b32 m0, s1
	v_exp_f32_e32 v58, v22
	v_exp_f32_e32 v59, v23
	v_exp_f32_e32 v60, v24
	v_exp_f32_e32 v61, v25
	v_exp_f32_e32 v62, v26
	v_exp_f32_e32 v63, v27
	v_exp_f32_e32 v64, v28
	v_exp_f32_e32 v65, v29
	v_exp_f32_e32 v94, v30
	v_exp_f32_e32 v95, v31
	v_exp_f32_e32 v96, v32
	v_exp_f32_e32 v97, v33
	v_exp_f32_e32 v131, v40
	v_exp_f32_e32 v132, v41
	v_exp_f32_e32 v133, v42
	v_exp_f32_e32 v134, v43
	v_exp_f32_e32 v135, v44
	v_exp_f32_e32 v136, v45
	v_exp_f32_e32 v137, v46
	v_exp_f32_e32 v146, v47
	ds_read_b128 v[22:25], v194 offset:8192
	ds_read_b128 v[26:29], v194 offset:8704
	ds_read_b128 v[30:33], v194 offset:10240
	ds_read_b128 v[40:43], v194 offset:10752
	ds_read_b128 v[44:47], v194 offset:12288
	ds_read_b128 v[82:85], v194 offset:12800
	ds_read_b128 v[86:89], v194 offset:14336
	ds_read_b128 v[90:93], v194 offset:14848
	v_exp_f32_e32 v56, v20
	v_exp_f32_e32 v57, v21
	v_exp_f32_e32 v130, v37
	s_waitcnt vmcnt(2) lgkmcnt(0)
	s_barrier
	v_cmp_gt_u32_e64 s[0:1], 32, v184
	v_exp_f32_e32 v48, v48
	v_exp_f32_e32 v49, v49
	v_exp_f32_e32 v147, v50
	v_exp_f32_e32 v148, v51
	v_exp_f32_e32 v149, v52
	v_exp_f32_e32 v150, v53
	v_exp_f32_e32 v151, v36
	ds_read_b64_tr_b16 v[18:19], v191 offset:24576
	ds_read_b64_tr_b16 v[20:21], v191 offset:25088
	s_waitcnt lgkmcnt(9)
	v_mfma_f32_32x32x16_bf16 v[98:113], v[22:25], v[142:145], v[2:17]
	v_add_f32_e32 v34, v54, v55
	v_add_f32_e32 v34, v34, v56
	v_add_f32_e32 v34, v34, v57
	v_add_f32_e32 v34, v34, v58
	v_add_f32_e32 v50, v34, v59
	v_cvt_pk_bf16_f32 v126, v54, v55
	v_cvt_pk_bf16_f32 v127, v56, v57
	ds_read_b64_tr_b16 v[34:35], v191 offset:28672
	ds_read_b64_tr_b16 v[36:37], v191 offset:29184
	s_waitcnt lgkmcnt(10)
	v_mfma_f32_32x32x16_bf16 v[66:81], v[26:29], v[142:145], v[2:17]
	v_add_f32_e32 v22, v60, v50
	v_add_f32_e32 v22, v61, v22
	v_add_f32_e32 v22, v62, v22
	v_add_f32_e32 v22, v63, v22
	v_cvt_pk_bf16_f32 v128, v58, v59
	v_cvt_pk_bf16_f32 v129, v60, v61
	ds_read_b64_tr_b16 v[50:51], v191 offset:25600
	ds_read_b64_tr_b16 v[52:53], v191 offset:26112
	s_waitcnt lgkmcnt(11)
	v_mfma_f32_32x32x16_bf16 v[98:113], v[30:33], v[138:141], v[98:113]
	v_add_f32_e32 v22, v64, v22
	v_add_f32_e32 v22, v65, v22
	v_add_f32_e32 v22, v94, v22
	v_add_f32_e32 v22, v95, v22
	v_cvt_pk_bf16_f32 v122, v62, v63
	v_cvt_pk_bf16_f32 v123, v64, v65
	ds_read_b64_tr_b16 v[54:55], v191 offset:29696
	ds_read_b64_tr_b16 v[56:57], v191 offset:30208
	s_waitcnt lgkmcnt(12)
	v_mfma_f32_32x32x16_bf16 v[66:81], v[40:43], v[138:141], v[66:81]
	v_add_f32_e32 v22, v96, v22
	v_add_f32_e32 v22, v97, v22
	v_add_f32_e32 v22, v130, v22
	v_add_f32_e32 v22, v131, v22
	v_cvt_pk_bf16_f32 v124, v94, v95
	v_cvt_pk_bf16_f32 v125, v96, v97
	ds_read_b64_tr_b16 v[58:59], v191 offset:26624
	ds_read_b64_tr_b16 v[60:61], v191 offset:27136
	s_waitcnt lgkmcnt(13)
	v_mfma_f32_32x32x16_bf16 v[98:113], v[44:47], v[118:121], v[98:113]
	v_add_f32_e32 v22, v132, v22
	v_add_f32_e32 v22, v133, v22
	v_add_f32_e32 v22, v134, v22
	v_add_f32_e32 v22, v135, v22
	v_cvt_pk_bf16_f32 v130, v130, v131
	v_cvt_pk_bf16_f32 v131, v132, v133
	ds_read_b64_tr_b16 v[62:63], v191 offset:30720
	ds_read_b64_tr_b16 v[64:65], v191 offset:31232
	s_waitcnt lgkmcnt(14)
	v_mfma_f32_32x32x16_bf16 v[66:81], v[82:85], v[118:121], v[66:81]
	v_add_f32_e32 v22, v136, v22
	v_add_f32_e32 v22, v137, v22
	v_add_f32_e32 v22, v146, v22
	v_add_f32_e32 v22, v48, v22
	v_cvt_pk_bf16_f32 v132, v134, v135
	v_cvt_pk_bf16_f32 v133, v136, v137
	ds_read_b64_tr_b16 v[82:83], v191 offset:27648
	ds_read_b64_tr_b16 v[84:85], v191 offset:28160
	s_waitcnt lgkmcnt(14)
	v_mfma_f32_32x32x16_bf16 v[98:113], v[86:89], v[114:117], v[98:113]
	v_add_f32_e32 v22, v49, v22
	v_add_f32_e32 v22, v147, v22
	v_add_f32_e32 v22, v148, v22
	v_add_f32_e32 v22, v149, v22
	v_cvt_pk_bf16_f32 v134, v146, v48
	v_cvt_pk_bf16_f32 v135, v49, v147
	ds_read_b64_tr_b16 v[86:87], v191 offset:31744
	ds_read_b64_tr_b16 v[88:89], v191 offset:32256
	v_mfma_f32_32x32x16_bf16 v[66:81], v[90:93], v[114:117], v[66:81]
	v_add_f32_e32 v22, v150, v22
	v_add_f32_e32 v22, v151, v22
	v_cvt_pk_bf16_f32 v136, v148, v149
	v_cvt_pk_bf16_f32 v137, v150, v151
	s_mov_b64 s[6:7], 0x1b1400
	v_add_f32_e32 v195, 0, v22
	v_lshl_add_u64 v[22:23], v[38:39], 0, s[6:7]
	s_add_i32 s4, s4, 0xa000
	s_mov_b32 s5, m0
	s_mov_b32 m0, s4
	s_nop 0
	global_load_lds_dwordx4 v[22:23], off
	s_mov_b32 m0, s5
	v_max_f32_e32 v22, v98, v99
	v_max3_f32 v23, v100, v101, v67
	v_max3_f32 v22, v22, v66, v68
	v_max3_f32 v22, v22, v69, v102
	v_max3_f32 v23, v23, v104, v105
	v_max3_f32 v22, v22, v103, v70
	v_max3_f32 v23, v23, v72, v73
	v_max3_f32 v22, v22, v71, v106
	v_max3_f32 v23, v23, v108, v109
	v_max3_f32 v22, v22, v107, v74
	v_max3_f32 v23, v23, v76, v77
	v_max3_f32 v22, v22, v75, v110
	v_max3_f32 v23, v23, v112, v113
	v_max3_f32 v22, v22, v111, v78
	v_max3_f32 v23, v23, v80, v81
	v_max3_f32 v22, v22, v79, v23
	v_mov_b32_e32 v23, v22
	s_nop 1
	v_permlane32_swap_b32_e32 v22, v23
	v_max_f32_e32 v22, v22, v23
	v_cmp_lt_f32_e32 vcc, s22, v22
	s_cmp_lg_u64 vcc, 0
	s_cselect_b64 s[4:5], -1, 0
	s_cbranch_vccnz .LBB0_2217

.LBB0_1268:
	ds_read_b64_tr_b16 v[150:151], v191 offset:32768
	ds_read_b64_tr_b16 v[152:153], v191 offset:33280
	s_waitcnt lgkmcnt(9)
	v_mfma_f32_32x32x16_bf16 v[82:97], v[146:149], v[142:145], v[2:17]
	v_add_f32_e32 v50, v98, v99
	v_add_f32_e32 v50, v100, v50
	v_add_f32_e32 v50, v101, v50
	v_add_f32_e32 v50, v102, v50
	v_add_f32_e32 v50, v103, v50
	v_cvt_pk_bf16_f32 v126, v98, v99
	v_cvt_pk_bf16_f32 v127, v100, v101
	ds_read_b64_tr_b16 v[146:147], v191 offset:36864
	ds_read_b64_tr_b16 v[148:149], v191 offset:37376
	v_add_f32_e32 v50, v104, v50
	v_add_f32_e32 v50, v105, v50
	v_add_f32_e32 v50, v106, v50
	v_add_f32_e32 v122, v107, v50
	s_waitcnt lgkmcnt(10)
	v_mfma_f32_32x32x16_bf16 v[50:65], v[174:177], v[142:145], v[2:17]
	v_cvt_pk_bf16_f32 v128, v102, v103
	v_cvt_pk_bf16_f32 v129, v104, v105
	ds_read_b64_tr_b16 v[98:99], v191 offset:33792
	ds_read_b64_tr_b16 v[100:101], v191 offset:34304
	s_waitcnt lgkmcnt(11)
	v_mfma_f32_32x32x16_bf16 v[82:97], v[178:181], v[138:141], v[82:97]
	v_add_f32_e32 v102, v108, v122
	v_add_f32_e32 v102, v109, v102
	v_add_f32_e32 v102, v110, v102
	v_add_f32_e32 v130, v111, v102
	v_cvt_pk_bf16_f32 v122, v106, v107
	v_cvt_pk_bf16_f32 v123, v108, v109
	ds_read_b64_tr_b16 v[102:103], v191 offset:37888
	ds_read_b64_tr_b16 v[104:105], v191 offset:38400
	s_waitcnt lgkmcnt(12)
	v_mfma_f32_32x32x16_bf16 v[50:65], v[170:173], v[138:141], v[50:65]
	v_add_f32_e32 v106, v112, v130
	v_add_f32_e32 v106, v113, v106
	v_add_f32_e32 v106, v66, v106
	v_add_f32_e32 v130, v67, v106
	v_cvt_pk_bf16_f32 v124, v110, v111
	v_cvt_pk_bf16_f32 v125, v112, v113
	ds_read_b64_tr_b16 v[106:107], v191 offset:34816
	ds_read_b64_tr_b16 v[108:109], v191 offset:35328
	s_waitcnt lgkmcnt(13)
	v_mfma_f32_32x32x16_bf16 v[82:97], v[166:169], v[118:121], v[82:97]
	v_add_f32_e32 v110, v68, v130
	v_add_f32_e32 v110, v69, v110
	v_add_f32_e32 v110, v70, v110
	v_add_f32_e32 v110, v71, v110
	v_cvt_pk_bf16_f32 v130, v66, v67
	v_cvt_pk_bf16_f32 v131, v68, v69
	ds_read_b64_tr_b16 v[66:67], v191 offset:38912
	ds_read_b64_tr_b16 v[68:69], v191 offset:39424
	s_waitcnt lgkmcnt(14)
	v_mfma_f32_32x32x16_bf16 v[50:65], v[162:165], v[118:121], v[50:65]
	v_add_f32_e32 v110, v72, v110
	v_add_f32_e32 v110, v73, v110
	v_add_f32_e32 v110, v74, v110
	v_add_f32_e32 v110, v75, v110
	v_cvt_pk_bf16_f32 v132, v70, v71
	v_cvt_pk_bf16_f32 v133, v72, v73
	ds_read_b64_tr_b16 v[70:71], v191 offset:35840
	ds_read_b64_tr_b16 v[72:73], v191 offset:36352
	s_waitcnt lgkmcnt(14)
	v_mfma_f32_32x32x16_bf16 v[82:97], v[158:161], v[114:117], v[82:97]
	v_add_f32_e32 v110, v76, v110
	v_add_f32_e32 v110, v77, v110
	v_add_f32_e32 v110, v78, v110
	v_add_f32_e32 v110, v79, v110
	v_cvt_pk_bf16_f32 v134, v74, v75
	v_cvt_pk_bf16_f32 v135, v76, v77
	ds_read_b64_tr_b16 v[74:75], v191 offset:39936
	ds_read_b64_tr_b16 v[76:77], v191 offset:40448
	v_mfma_f32_32x32x16_bf16 v[50:65], v[154:157], v[114:117], v[50:65]
	v_add_f32_e32 v110, v80, v110
	v_add_f32_e32 v110, v81, v110
	v_cvt_pk_bf16_f32 v136, v78, v79
	v_cvt_pk_bf16_f32 v137, v80, v81
	s_mov_b64 s[4:5], 0x288000
	v_lshl_add_u64 v[78:79], v[182:183], 0, s[4:5]
	s_mov_b32 s4, m0
	s_mov_b32 m0, s13
	s_nop 0
	global_load_lds_dwordx4 v[78:79], off
	s_mov_b32 m0, s4
	v_max_f32_e32 v78, v82, v83
	s_nop 1
	v_max3_f32 v79, v84, v85, v51
	v_max3_f32 v78, v78, v50, v52
	v_max3_f32 v78, v78, v53, v86
	v_max3_f32 v79, v79, v88, v89
	v_max3_f32 v78, v78, v87, v54
	v_max3_f32 v79, v79, v56, v57
	v_max3_f32 v78, v78, v55, v90
	v_max3_f32 v79, v79, v92, v93
	v_max3_f32 v78, v78, v91, v58
	v_max3_f32 v79, v79, v60, v61
	v_max3_f32 v78, v78, v59, v94
	v_max3_f32 v79, v79, v96, v97
	v_max3_f32 v78, v78, v95, v62
	v_max3_f32 v79, v79, v64, v65
	v_max3_f32 v78, v78, v63, v79
	v_mov_b32_e32 v79, v78
	s_nop 1
	v_permlane32_swap_b32_e32 v78, v79
	v_max_f32_e32 v78, v78, v79
	v_cmp_lt_f32_e32 vcc, s22, v78
	s_cmp_lg_u64 vcc, 0
	v_add_f32_e32 v170, v195, v110
	s_cselect_b64 s[4:5], -1, 0
	s_cbranch_vccnz .LBB0_2220

.LBB0_1271:
	ds_read_b64_tr_b16 v[98:99], v191 offset:40960
	ds_read_b64_tr_b16 v[100:101], v191 offset:41472
	v_add_f32_e32 v66, v82, v83
	v_add_f32_e32 v66, v84, v66
	v_add_f32_e32 v66, v85, v66
	v_add_f32_e32 v66, v86, v66
	v_add_f32_e32 v106, v87, v66
	s_waitcnt lgkmcnt(9)
	v_mfma_f32_32x32x16_bf16 v[66:81], v[166:169], v[142:145], v[2:17]
	v_cvt_pk_bf16_f32 v126, v82, v83
	v_cvt_pk_bf16_f32 v127, v84, v85
	ds_read_b64_tr_b16 v[82:83], v191 offset:45056
	ds_read_b64_tr_b16 v[84:85], v191 offset:45568
	s_waitcnt lgkmcnt(10)
	v_mfma_f32_32x32x16_bf16 v[2:17], v[162:165], v[142:145], v[2:17]
	v_add_f32_e32 v106, v88, v106
	v_add_f32_e32 v106, v89, v106
	v_add_f32_e32 v106, v90, v106
	v_add_f32_e32 v106, v91, v106
	v_cvt_pk_bf16_f32 v128, v86, v87
	v_cvt_pk_bf16_f32 v129, v88, v89
	ds_read_b64_tr_b16 v[86:87], v191 offset:41984
	ds_read_b64_tr_b16 v[88:89], v191 offset:42496
	s_waitcnt lgkmcnt(11)
	v_mfma_f32_32x32x16_bf16 v[66:81], v[158:161], v[138:141], v[66:81]
	v_add_f32_e32 v106, v92, v106
	v_add_f32_e32 v106, v93, v106
	v_add_f32_e32 v106, v94, v106
	v_add_f32_e32 v106, v95, v106
	v_cvt_pk_bf16_f32 v122, v90, v91
	v_cvt_pk_bf16_f32 v123, v92, v93
	ds_read_b64_tr_b16 v[90:91], v191 offset:46080
	ds_read_b64_tr_b16 v[92:93], v191 offset:46592
	s_waitcnt lgkmcnt(12)
	v_mfma_f32_32x32x16_bf16 v[2:17], v[154:157], v[138:141], v[2:17]
	v_add_f32_e32 v106, v96, v106
	v_add_f32_e32 v106, v97, v106
	v_add_f32_e32 v106, v50, v106
	v_add_f32_e32 v106, v51, v106
	v_cvt_pk_bf16_f32 v124, v94, v95
	v_cvt_pk_bf16_f32 v125, v96, v97
	ds_read_b64_tr_b16 v[94:95], v191 offset:43008
	ds_read_b64_tr_b16 v[96:97], v191 offset:43520
	s_waitcnt lgkmcnt(13)
	v_mfma_f32_32x32x16_bf16 v[66:81], v[102:105], v[118:121], v[66:81]
	v_add_f32_e32 v102, v52, v106
	v_add_f32_e32 v102, v53, v102
	v_add_f32_e32 v102, v54, v102
	v_add_f32_e32 v106, v55, v102
	v_cvt_pk_bf16_f32 v130, v50, v51
	v_cvt_pk_bf16_f32 v131, v52, v53
	ds_read_b64_tr_b16 v[102:103], v191 offset:47104
	ds_read_b64_tr_b16 v[104:105], v191 offset:47616
	s_waitcnt lgkmcnt(14)
	v_mfma_f32_32x32x16_bf16 v[2:17], v[150:153], v[118:121], v[2:17]
	v_add_f32_e32 v50, v56, v106
	v_add_f32_e32 v50, v57, v50
	v_add_f32_e32 v50, v58, v50
	v_add_f32_e32 v50, v59, v50
	v_cvt_pk_bf16_f32 v132, v54, v55
	v_cvt_pk_bf16_f32 v133, v56, v57
	ds_read_b64_tr_b16 v[106:107], v191 offset:44032
	ds_read_b64_tr_b16 v[108:109], v191 offset:44544
	s_waitcnt lgkmcnt(14)
	v_mfma_f32_32x32x16_bf16 v[66:81], v[146:149], v[114:117], v[66:81]
	v_add_f32_e32 v50, v60, v50
	v_add_f32_e32 v50, v61, v50
	v_add_f32_e32 v50, v62, v50
	v_add_f32_e32 v50, v63, v50
	v_cvt_pk_bf16_f32 v134, v58, v59
	v_cvt_pk_bf16_f32 v135, v60, v61
	ds_read_b64_tr_b16 v[118:119], v191 offset:48128
	ds_read_b64_tr_b16 v[120:121], v191 offset:48640
	v_mfma_f32_32x32x16_bf16 v[2:17], v[110:113], v[114:117], v[2:17]
	v_add_f32_e32 v50, v64, v50
	v_add_f32_e32 v50, v65, v50
	v_cvt_pk_bf16_f32 v136, v62, v63
	v_cvt_pk_bf16_f32 v137, v64, v65
	v_max_f32_e32 v51, v66, v67
	s_nop 3
	s_nop 2
	v_max3_f32 v52, v68, v69, v3
	v_max3_f32 v51, v51, v2, v4
	v_max3_f32 v51, v51, v5, v70
	v_max3_f32 v52, v52, v72, v73
	v_max3_f32 v51, v51, v71, v6
	v_max3_f32 v52, v52, v8, v9
	v_max3_f32 v51, v51, v7, v74
	v_max3_f32 v52, v52, v76, v77
	v_max3_f32 v51, v51, v75, v10
	v_max3_f32 v52, v52, v12, v13
	v_max3_f32 v51, v51, v11, v78
	v_max3_f32 v52, v52, v80, v81
	v_max3_f32 v51, v51, v79, v14
	v_max3_f32 v52, v52, v16, v17
	v_add_f32_e32 v110, v170, v50
	v_max3_f32 v50, v51, v15, v52
	v_mov_b32_e32 v51, v50
	s_nop 1
	v_permlane32_swap_b32_e32 v50, v51
	v_max_f32_e32 v50, v50, v51
	v_cmp_lt_f32_e32 vcc, s22, v50
	s_cmp_lg_u64 vcc, 0
	s_cselect_b64 s[4:5], -1, 0
	s_cbranch_vccnz .LBB0_2223

.LBB0_1280:
	v_readlane_b32 s0, v252, 42
	s_lshl_b32 s10, s0, 1
	s_add_u32 s0, s9, s10
	s_addc_u32 s11, s11, 0
	v_readlane_b32 s6, v253, 50
	s_add_u32 s4, s81, s6
	s_addc_u32 s5, s83, 0
	s_add_u32 s6, s74, s6
	s_addc_u32 s7, s75, 0
	v_and_b32_e32 v184, 63, v36
	s_lshl_b32 s9, s8, 5
	s_mul_i32 s12, s8, 0x6c000
	s_mul_hi_i32 s13, s9, 0x3600
	s_add_u32 s12, s0, s12
	v_lshlrev_b32_e32 v0, 8, v184
	s_addc_u32 s13, s11, s13
	v_lshl_add_u64 v[4:5], s[4:5], 0, v[0:1]
	s_lshl_b32 s4, s8, 3
	s_ashr_i32 s5, s4, 31
	s_and_b32 s0, s1, 0x3fffffc0
	v_lshl_add_u64 v[34:35], s[4:5], 1, v[4:5]
	s_lshl_b32 s4, s8, 4
	v_bfe_u32 v0, v36, 2, 4
	s_ashr_i32 s1, s1, 3
	v_and_or_b32 v0, s4, 48, v0
	s_and_b32 s4, s1, 0xffffffe0
	v_lshlrev_b32_e32 v0, 8, v0
	s_ashr_i32 s5, s4, 31
	v_lshlrev_b32_e32 v185, 3, v2
	s_lshl_b32 s1, s8, 10
	v_lshl_add_u64 v[4:5], s[6:7], 0, v[0:1]
	v_and_b32_e32 v188, 24, v185
	s_cmp_lg_u32 0, -1
	v_and_b32_e32 v186, 31, v36
	v_lshl_add_u64 v[4:5], s[4:5], 1, v[4:5]
	v_lshlrev_b32_e32 v0, 1, v188
	s_cselect_b32 s4, 0, 0
	v_lshl_add_u64 v[182:183], v[4:5], 0, v[0:1]
	s_add_i32 s4, s4, s1
	s_mov_b32 s1, m0
	s_mov_b32 m0, s4
	s_nop 0
	global_load_lds_dwordx4 v[34:35], off
	s_mov_b32 m0, s1
	v_mul_u32_u24_e32 v0, 0x1b00, v186
	v_bfe_u32 v187, v36, 5, 1
	s_add_i32 s11, s4, 0x6000
	s_mov_b32 s1, m0
	s_mov_b32 m0, s11
	s_nop 0
	global_load_lds_dwordx4 v[182:183], off
	s_mov_b32 m0, s1
	v_lshlrev_b32_e32 v0, 1, v0
	s_mov_b64 s[6:7], 0x4000
	s_add_i32 s1, s4, 0x2000
	v_lshl_or_b32 v0, v187, 4, v0
	v_lshl_add_u64 v[2:3], v[34:35], 0, s[6:7]
	s_mov_b32 s5, m0
	s_mov_b32 m0, s1
	s_nop 0
	global_load_lds_dwordx4 v[2:3], off
	s_mov_b32 m0, s5
	v_lshl_add_u64 v[14:15], s[12:13], 0, v[0:1]
	s_mov_b64 s[12:13], 0x1800
	s_movk_i32 s1, 0x1000
	v_lshl_add_u64 v[10:11], v[14:15], 0, s[12:13]
	v_add_co_u32_e32 v14, vcc, s1, v14
	global_load_dwordx4 v[2:5], v[10:11], off offset:96
	global_load_dwordx4 v[6:9], v[10:11], off offset:64
	s_nop 0
	global_load_dwordx4 v[10:13], v[10:11], off offset:32
	v_addc_co_u32_e32 v15, vcc, 0, v15, vcc
	global_load_dwordx4 v[14:17], v[14:15], off offset:2048
	v_readlane_b32 s40, v253, 26
	v_and_b32_e32 v37, 32, v36
	v_readlane_b32 s44, v253, 30
	v_readlane_b32 s45, v253, 31
	s_nop 4
	global_load_dwordx4 v[18:21], v37, s[44:45] offset:208
	global_load_dwordx4 v[22:25], v37, s[44:45] offset:192
	global_load_dwordx4 v[26:29], v37, s[44:45] offset:144
	global_load_dwordx4 v[30:33], v37, s[44:45] offset:128
	global_load_dwordx4 v[38:41], v37, s[44:45] offset:80
	global_load_dwordx4 v[42:45], v37, s[44:45] offset:64
	global_load_dwordx4 v[46:49], v37, s[44:45] offset:16
	global_load_dwordx4 v[50:53], v37, s[44:45]
	v_lshlrev_b32_e32 v0, 1, v36
	v_and_b32_e32 v189, 32, v0
	s_mov_b32 s1, 0x800000
	s_lshl_b32 s0, s0, 2
	s_add_i32 s12, s0, 0
	v_lshl_add_u32 v190, v186, 2, s12
	v_readlane_b32 s41, v253, 27
	v_readlane_b32 s42, v253, 28
	v_readlane_b32 s43, v253, 29
	v_readlane_b32 s46, v253, 32
	v_readlane_b32 s47, v253, 33
	s_waitcnt vmcnt(11)
	v_and_b32_e32 v55, 0xffff0000, v2
	v_lshlrev_b32_e32 v54, 16, v2
	s_waitcnt vmcnt(9)
	v_and_b32_e32 v67, 0xffff0000, v13
	v_lshlrev_b32_e32 v66, 16, v13
	v_and_b32_e32 v57, 0xffff0000, v3
	s_waitcnt vmcnt(8)
	v_and_b32_e32 v13, 0xffff0000, v14
	v_lshlrev_b32_e32 v56, 16, v3
	v_and_b32_e32 v3, 0xffff0000, v4
	v_lshlrev_b32_e32 v2, 16, v4
	v_and_b32_e32 v59, 0xffff0000, v5
	v_lshlrev_b32_e32 v58, 16, v5
	v_and_b32_e32 v5, 0xffff0000, v6
	v_lshlrev_b32_e32 v4, 16, v6
	v_and_b32_e32 v61, 0xffff0000, v7
	v_lshlrev_b32_e32 v60, 16, v7
	v_and_b32_e32 v7, 0xffff0000, v8
	v_lshlrev_b32_e32 v6, 16, v8
	v_and_b32_e32 v63, 0xffff0000, v9
	v_lshlrev_b32_e32 v62, 16, v9
	v_and_b32_e32 v9, 0xffff0000, v10
	v_lshlrev_b32_e32 v8, 16, v10
	v_and_b32_e32 v65, 0xffff0000, v11
	v_lshlrev_b32_e32 v64, 16, v11
	v_and_b32_e32 v11, 0xffff0000, v12
	v_lshlrev_b32_e32 v10, 16, v12
	v_lshlrev_b32_e32 v12, 16, v14
	v_mul_f32_e32 v0, v13, v13
	v_and_b32_e32 v69, 0xffff0000, v15
	v_lshlrev_b32_e32 v68, 16, v15
	v_pk_fma_f32 v[70:71], v[12:13], v[12:13], v[0:1] op_sel_hi:[1,1,0]
	v_and_b32_e32 v15, 0xffff0000, v16
	v_mul_f32_e32 v14, v69, v69
	v_pk_fma_f32 v[70:71], v[68:69], v[68:69], v[70:71]
	v_mul_f32_e32 v0, v15, v15
	v_pk_add_f32 v[70:71], v[14:15], v[70:71] op_sel_hi:[0,1]
	v_lshlrev_b32_e32 v14, 16, v16
	v_pk_fma_f32 v[70:71], v[14:15], v[14:15], v[70:71]
	v_and_b32_e32 v73, 0xffff0000, v17
	v_pk_add_f32 v[70:71], v[0:1], v[70:71] op_sel_hi:[0,1]
	v_lshlrev_b32_e32 v72, 16, v17
	v_pk_fma_f32 v[16:17], v[72:73], v[72:73], v[70:71]
	v_mul_f32_e32 v0, v73, v73
	v_pk_add_f32 v[16:17], v[0:1], v[16:17] op_sel_hi:[0,1]
	v_pk_fma_f32 v[16:17], v[8:9], v[8:9], v[16:17]
	v_mul_f32_e32 v0, v9, v9
	v_pk_add_f32 v[16:17], v[0:1], v[16:17] op_sel_hi:[0,1]
	v_pk_fma_f32 v[16:17], v[64:65], v[64:65], v[16:17]
	v_mul_f32_e32 v0, v65, v65
	v_pk_add_f32 v[16:17], v[0:1], v[16:17] op_sel_hi:[0,1]
	v_pk_fma_f32 v[16:17], v[10:11], v[10:11], v[16:17]
	v_mul_f32_e32 v0, v11, v11
	v_pk_add_f32 v[16:17], v[0:1], v[16:17] op_sel_hi:[0,1]
	v_pk_fma_f32 v[16:17], v[66:67], v[66:67], v[16:17]
	v_mul_f32_e32 v0, v67, v67
	v_pk_add_f32 v[16:17], v[0:1], v[16:17] op_sel_hi:[0,1]
	v_pk_fma_f32 v[16:17], v[4:5], v[4:5], v[16:17]
	v_mul_f32_e32 v0, v5, v5
	v_pk_add_f32 v[16:17], v[0:1], v[16:17] op_sel_hi:[0,1]
	v_pk_fma_f32 v[16:17], v[60:61], v[60:61], v[16:17]
	v_mul_f32_e32 v0, v61, v61
	v_pk_add_f32 v[16:17], v[0:1], v[16:17] op_sel_hi:[0,1]
	v_pk_fma_f32 v[16:17], v[6:7], v[6:7], v[16:17]
	v_mul_f32_e32 v0, v7, v7
	v_pk_add_f32 v[16:17], v[0:1], v[16:17] op_sel_hi:[0,1]
	v_pk_fma_f32 v[16:17], v[62:63], v[62:63], v[16:17]
	v_mul_f32_e32 v0, v63, v63
	v_pk_add_f32 v[16:17], v[0:1], v[16:17] op_sel_hi:[0,1]
	v_pk_fma_f32 v[16:17], v[54:55], v[54:55], v[16:17]
	v_mul_f32_e32 v0, v55, v55
	v_pk_add_f32 v[16:17], v[0:1], v[16:17] op_sel_hi:[0,1]
	v_pk_fma_f32 v[16:17], v[56:57], v[56:57], v[16:17]
	v_mul_f32_e32 v0, v57, v57
	v_pk_add_f32 v[16:17], v[0:1], v[16:17] op_sel_hi:[0,1]
	v_pk_fma_f32 v[16:17], v[2:3], v[2:3], v[16:17]
	v_mul_f32_e32 v0, v3, v3
	v_pk_add_f32 v[16:17], v[0:1], v[16:17] op_sel_hi:[0,1]
	v_pk_fma_f32 v[16:17], v[58:59], v[58:59], v[16:17]
	v_mul_f32_e32 v0, v59, v59
	v_pk_add_f32 v[16:17], v[0:1], v[16:17] op_sel_hi:[0,1]
	v_mov_b32_e32 v0, v16
	s_nop 1
	v_permlane32_swap_b32_e32 v16, v0
	v_add_f32_e32 v0, v16, v0
	v_fmamk_f32 v0, v0, 0x3c800000, v237
	v_mul_f32_e32 v16, 0x4b800000, v0
	v_cmp_gt_f32_e32 vcc, s1, v0
	v_lshl_add_u32 v17, v187, 10, 0
	s_add_i32 s1, s4, 0x4000
	v_cndmask_b32_e32 v0, v0, v16, vcc
	v_rsq_f32_e32 v0, v0
	v_lshlrev_b32_e32 v16, 4, v186
	v_add_u32_e32 v194, v17, v16
	v_mul_f32_e32 v16, 0x45800000, v0
	v_cndmask_b32_e32 v0, v0, v16, vcc
	v_pk_mul_f32 v[6:7], v[0:1], v[6:7] op_sel_hi:[0,1]
	v_pk_mul_f32 v[12:13], v[0:1], v[12:13] op_sel_hi:[0,1]
	v_pk_mul_f32 v[16:17], v[0:1], v[68:69] op_sel_hi:[0,1]
	v_pk_mul_f32 v[14:15], v[0:1], v[14:15] op_sel_hi:[0,1]
	s_waitcnt vmcnt(5)
	v_pk_mul_f32 v[6:7], v[6:7], v[26:27]
	v_pk_mul_f32 v[26:27], v[0:1], v[62:63] op_sel_hi:[0,1]
	v_pk_mul_f32 v[2:3], v[0:1], v[2:3] op_sel_hi:[0,1]
	s_waitcnt vmcnt(0)
	v_pk_mul_f32 v[12:13], v[50:51], v[12:13]
	v_pk_mul_f32 v[16:17], v[52:53], v[16:17]
	v_pk_mul_f32 v[14:15], v[46:47], v[14:15]
	v_pk_mul_f32 v[46:47], v[0:1], v[72:73] op_sel_hi:[0,1]
	v_pk_mul_f32 v[8:9], v[0:1], v[8:9] op_sel_hi:[0,1]
	v_pk_mul_f32 v[10:11], v[0:1], v[10:11] op_sel_hi:[0,1]
	v_pk_mul_f32 v[26:27], v[26:27], v[28:29]
	v_pk_mul_f32 v[28:29], v[0:1], v[54:55] op_sel_hi:[0,1]
	v_pk_mul_f32 v[52:53], v[2:3], v[18:19]
	v_pk_mul_f32 v[2:3], v[0:1], v[58:59] op_sel_hi:[0,1]
	v_pk_mul_f32 v[46:47], v[48:49], v[46:47]
	v_pk_mul_f32 v[8:9], v[42:43], v[8:9]
	v_pk_mul_f32 v[42:43], v[0:1], v[64:65] op_sel_hi:[0,1]
	v_pk_mul_f32 v[10:11], v[10:11], v[38:39]
	v_pk_mul_f32 v[38:39], v[0:1], v[66:67] op_sel_hi:[0,1]
	v_pk_mul_f32 v[48:49], v[28:29], v[22:23]
	v_pk_mul_f32 v[22:23], v[0:1], v[56:57] op_sel_hi:[0,1]
	v_pk_mul_f32 v[54:55], v[2:3], v[20:21]
	v_pk_mul_f32 v[2:3], v[12:13], s[14:15] op_sel_hi:[1,0]
	v_pk_mul_f32 v[12:13], v[16:17], s[14:15] op_sel_hi:[1,0]
	v_pk_mul_f32 v[42:43], v[44:45], v[42:43]
	v_pk_mul_f32 v[38:39], v[38:39], v[40:41]
	v_pk_mul_f32 v[4:5], v[0:1], v[4:5] op_sel_hi:[0,1]
	v_pk_mul_f32 v[50:51], v[22:23], v[24:25]
	v_pk_mul_f32 v[14:15], v[14:15], s[14:15] op_sel_hi:[1,0]
	v_pk_mul_f32 v[16:17], v[46:47], s[14:15] op_sel_hi:[1,0]
	v_bfe_u32 v21, v13, 16, 1
	v_bfe_u32 v22, v12, 16, 1
	v_bfe_u32 v23, v3, 16, 1
	v_bfe_u32 v24, v2, 16, 1
	v_pk_mul_f32 v[4:5], v[4:5], v[30:31]
	v_pk_mul_f32 v[30:31], v[0:1], v[60:61] op_sel_hi:[0,1]
	v_bfe_u32 v0, v17, 16, 1
	v_bfe_u32 v18, v16, 16, 1
	v_bfe_u32 v19, v15, 16, 1
	v_bfe_u32 v20, v14, 16, 1
	v_add3_u32 v24, v2, v24, s80
	v_add3_u32 v25, v3, v23, s80
	v_add3_u32 v28, v12, v22, s80
	v_add3_u32 v29, v13, v21, s80
	v_pk_mul_f32 v[2:3], v[8:9], s[14:15] op_sel_hi:[1,0]
	v_pk_mul_f32 v[8:9], v[42:43], s[14:15] op_sel_hi:[1,0]
	v_pk_mul_f32 v[10:11], v[10:11], s[14:15] op_sel_hi:[1,0]
	v_pk_mul_f32 v[12:13], v[38:39], s[14:15] op_sel_hi:[1,0]
	v_pk_mul_f32 v[30:31], v[30:31], v[32:33]
	v_add3_u32 v32, v14, v20, s80
	v_add3_u32 v33, v15, v19, s80
	v_add3_u32 v37, v16, v18, s80
	v_add3_u32 v58, v17, v0, s80
	v_bfe_u32 v0, v13, 16, 1
	v_bfe_u32 v14, v12, 16, 1
	v_bfe_u32 v15, v11, 16, 1
	v_bfe_u32 v16, v10, 16, 1
	v_bfe_u32 v17, v9, 16, 1
	v_bfe_u32 v18, v8, 16, 1
	v_bfe_u32 v19, v3, 16, 1
	v_bfe_u32 v20, v2, 16, 1
	v_add3_u32 v59, v2, v20, s80
	v_add3_u32 v60, v3, v19, s80
	v_add3_u32 v61, v8, v18, s80
	v_add3_u32 v62, v9, v17, s80
	v_add3_u32 v63, v10, v16, s80
	v_add3_u32 v64, v11, v15, s80
	v_add3_u32 v65, v12, v14, s80
	v_add3_u32 v66, v13, v0, s80
	v_pk_mul_f32 v[18:19], v[4:5], s[14:15] op_sel_hi:[1,0]
	v_pk_mul_f32 v[46:47], v[6:7], s[14:15] op_sel_hi:[1,0]
	v_mov_b32_e32 v2, v1
	v_mov_b32_e32 v3, v1
	v_mov_b32_e32 v4, v1
	v_mov_b32_e32 v5, v1
	v_mov_b32_e32 v6, v1
	v_mov_b32_e32 v7, v1
	v_mov_b32_e32 v8, v1
	v_mov_b32_e32 v9, v1
	v_mov_b32_e32 v10, v1
	v_mov_b32_e32 v11, v1
	v_mov_b32_e32 v12, v1
	v_mov_b32_e32 v13, v1
	v_mov_b32_e32 v14, v1
	v_mov_b32_e32 v15, v1
	v_mov_b32_e32 v0, v1
	v_mov_b64_e32 v[16:17], v[14:15]
	v_mov_b64_e32 v[14:15], v[12:13]
	v_mov_b64_e32 v[12:13], v[10:11]
	v_mov_b64_e32 v[10:11], v[8:9]
	v_mov_b64_e32 v[8:9], v[6:7]
	v_mov_b64_e32 v[6:7], v[4:5]
	v_mov_b64_e32 v[4:5], v[2:3]
	v_mov_b64_e32 v[2:3], v[0:1]
	v_lshl_add_u64 v[22:23], v[34:35], 0, s[24:25]
	s_mov_b32 s5, m0
	s_mov_b32 m0, s1
	s_nop 0
	global_load_lds_dwordx4 v[22:23], off
	s_mov_b32 m0, s5
	s_waitcnt vmcnt(3) lgkmcnt(0)
	s_barrier
	ds_read_b128 v[38:41], v194 offset:512
	ds_read_b128 v[42:45], v194
	v_pk_mul_f32 v[20:21], v[30:31], s[14:15] op_sel_hi:[1,0]
	s_mov_b32 s1, 0x7060302
	v_pk_mul_f32 v[56:57], v[26:27], s[14:15] op_sel_hi:[1,0]
	v_bfe_u32 v26, v21, 16, 1
	v_bfe_u32 v27, v20, 16, 1
	v_bfe_u32 v30, v19, 16, 1
	v_bfe_u32 v31, v18, 16, 1
	v_perm_b32 v145, v58, v37, s1
	v_perm_b32 v144, v33, v32, s1
	v_perm_b32 v143, v29, v28, s1
	v_perm_b32 v142, v25, v24, s1
	v_add3_u32 v0, v18, v31, s80
	v_add3_u32 v71, v19, v30, s80
	v_add3_u32 v72, v20, v27, s80
	v_add3_u32 v73, v21, v26, s80
	s_waitcnt lgkmcnt(0)
	v_mfma_f32_32x32x16_bf16 v[18:33], v[42:45], v[142:145], v[2:17]
	v_bfe_u32 v67, v57, 16, 1
	v_bfe_u32 v68, v56, 16, 1
	v_bfe_u32 v69, v47, 16, 1
	v_bfe_u32 v70, v46, 16, 1
	v_add3_u32 v37, v46, v70, s80
	v_add3_u32 v58, v47, v69, s80
	v_add3_u32 v68, v56, v68, s80
	v_mfma_f32_32x32x16_bf16 v[2:17], v[38:41], v[142:145], v[2:17]
	v_add3_u32 v67, v57, v67, s80
	v_mul_f32_e64 v56, v48, s14
	v_mul_f32_e64 v57, v49, s14
	ds_read_b128 v[42:45], v194 offset:2560
	ds_read_b128 v[46:49], v194 offset:2048
	v_perm_b32 v141, v66, v65, s1
	v_perm_b32 v140, v64, v63, s1
	v_perm_b32 v139, v62, v61, s1
	v_perm_b32 v138, v60, v59, s1
	v_perm_b32 v137, v67, v68, s1
	v_perm_b32 v136, v58, v37, s1
	s_waitcnt lgkmcnt(0)
	v_mfma_f32_32x32x16_bf16 v[18:33], v[46:49], v[138:141], v[18:33]
	ds_read_b128 v[38:41], v194 offset:4608
	ds_read_b128 v[46:49], v194 offset:4096
	v_perm_b32 v135, v73, v72, s1
	v_perm_b32 v134, v71, v0, s1
	v_mul_f32_e64 v50, v50, s14
	v_mul_f32_e64 v51, v51, s14
	v_pk_mul_f32 v[52:53], v[52:53], s[14:15] op_sel_hi:[1,0]
	v_pk_mul_f32 v[54:55], v[54:55], s[14:15] op_sel_hi:[1,0]
	v_bfe_u32 v61, v53, 16, 1
	v_mfma_f32_32x32x16_bf16 v[2:17], v[42:45], v[138:141], v[2:17]
	v_bfe_u32 v42, v50, 16, 1
	v_bfe_u32 v43, v57, 16, 1
	v_bfe_u32 v44, v56, 16, 1
	v_add3_u32 v0, v56, v44, s80
	v_add3_u32 v37, v57, v43, s80
	v_add3_u32 v50, v50, v42, s80
	v_bfe_u32 v59, v55, 16, 1
	s_waitcnt lgkmcnt(0)
	v_mfma_f32_32x32x16_bf16 v[18:33], v[46:49], v[134:137], v[18:33]
	ds_read_b128 v[42:45], v194 offset:6656
	ds_read_b128 v[46:49], v194 offset:6144
	v_bfe_u32 v60, v54, 16, 1
	v_bfe_u32 v62, v52, 16, 1
	v_bfe_u32 v63, v51, 16, 1
	v_add3_u32 v51, v51, v63, s80
	v_add3_u32 v52, v52, v62, s80
	v_perm_b32 v126, v37, v0, s1
	v_mfma_f32_32x32x16_bf16 v[2:17], v[38:41], v[134:137], v[2:17]
	v_add3_u32 v38, v53, v61, s80
	v_add3_u32 v39, v54, v60, s80
	v_add3_u32 v40, v55, v59, s80
	v_lshlrev_b32_e32 v0, 4, v36
	v_perm_b32 v129, v40, v39, s1
	v_perm_b32 v128, v38, v52, s1
	v_perm_b32 v127, v51, v50, s1
	v_and_b32_e32 v0, 0xc0, v0
	v_lshl_or_b32 v0, v187, 8, v0
	s_waitcnt lgkmcnt(0)
	v_mfma_f32_32x32x16_bf16 v[18:33], v[46:49], v[126:129], v[18:33]
	v_add3_u32 v36, 0, v189, v188
	v_add_u32_e32 v192, v36, v0
	s_mov_b64 s[0:1], 0xc000
	v_mfma_f32_32x32x16_bf16 v[2:17], v[42:45], v[126:129], v[2:17]
	s_nop 15
	s_nop 7
	s_nop 0
	v_max3_f32 v36, v18, v19, v2
	v_max3_f32 v37, v20, v21, v3
	s_nop 0
	v_max3_f32 v36, v36, v4, v5
	v_max3_f32 v37, v37, v24, v25
	s_nop 0
	v_max3_f32 v36, v36, v22, v23
	v_max3_f32 v37, v37, v8, v9
	s_nop 0
	v_max3_f32 v36, v36, v6, v7
	v_max3_f32 v37, v37, v28, v29
	s_nop 0
	v_max3_f32 v36, v36, v26, v27
	v_max3_f32 v37, v37, v12, v13
	s_nop 0
	v_max3_f32 v36, v36, v10, v11
	v_max3_f32 v37, v37, v32, v33
	s_nop 0
	v_max3_f32 v36, v36, v30, v31
	v_max3_f32 v37, v37, v16, v17
	s_nop 0
	v_max3_f32 v36, v36, v14, v15
	s_nop 0
	v_max_f32_e32 v36, v36, v37
	s_nop 0
	v_mov_b32_e32 v37, v36
	s_nop 1
	v_permlane32_swap_b32_e32 v36, v37
	v_max_f32_e32 v36, v36, v37
	s_nop 0
	v_add_f32_e32 v191, v1, v36
	v_sub_f32_e32 v37, v2, v36
	v_sub_f32_e32 v18, v18, v36
	v_sub_f32_e32 v19, v19, v36
	v_sub_f32_e32 v38, v3, v36
	v_sub_f32_e32 v20, v20, v36
	s_nop 0
	v_xor_b32_e32 v2, 0x80000000, v191
	v_sub_f32_e32 v39, v4, v36
	v_sub_f32_e32 v21, v21, v36
	v_sub_f32_e32 v40, v5, v36
	v_sub_f32_e32 v22, v22, v36
	v_sub_f32_e32 v41, v6, v36
	v_sub_f32_e32 v23, v23, v36
	v_sub_f32_e32 v42, v7, v36
	v_sub_f32_e32 v24, v24, v36
	v_sub_f32_e32 v43, v8, v36
	v_sub_f32_e32 v25, v25, v36
	v_sub_f32_e32 v44, v9, v36
	v_sub_f32_e32 v26, v26, v36
	v_sub_f32_e32 v45, v10, v36
	v_sub_f32_e32 v27, v27, v36
	v_sub_f32_e32 v46, v11, v36
	v_sub_f32_e32 v28, v28, v36
	v_sub_f32_e32 v47, v12, v36
	v_sub_f32_e32 v29, v29, v36
	v_sub_f32_e32 v48, v13, v36
	v_sub_f32_e32 v30, v30, v36
	v_sub_f32_e32 v49, v14, v36
	v_sub_f32_e32 v31, v31, v36
	v_sub_f32_e32 v50, v15, v36
	v_sub_f32_e32 v32, v32, v36
	v_sub_f32_e32 v51, v16, v36
	v_sub_f32_e32 v33, v33, v36
	v_sub_f32_e32 v36, v17, v36
	v_mov_b32_e32 v3, v2
	v_mov_b32_e32 v4, v2
	v_mov_b32_e32 v5, v2
	v_mov_b32_e32 v6, v2
	v_mov_b32_e32 v7, v2
	v_mov_b32_e32 v8, v2
	v_mov_b32_e32 v9, v2
	v_mov_b32_e32 v10, v2
	v_mov_b32_e32 v11, v2
	v_mov_b32_e32 v12, v2
	v_mov_b32_e32 v13, v2
	v_mov_b32_e32 v14, v2
	v_mov_b32_e32 v15, v2
	v_mov_b32_e32 v16, v2
	v_mov_b32_e32 v17, v2
	s_waitcnt vmcnt(0) lgkmcnt(0)
	s_barrier
	v_exp_f32_e32 v52, v18
	v_exp_f32_e32 v53, v19
	v_lshl_add_u64 v[18:19], v[34:35], 0, s[0:1]
	s_mov_b32 s0, m0
	s_mov_b32 m0, s4
	s_nop 0
	global_load_lds_dwordx4 v[18:19], off
	s_mov_b32 m0, s0
	v_lshl_add_u64 v[18:19], v[182:183], 0, s[6:7]
	s_add_i32 s0, s4, 0x8000
	s_mov_b32 s1, m0
	s_mov_b32 m0, s0
	s_nop 0
	global_load_lds_dwordx4 v[18:19], off
	s_mov_b32 m0, s1
	v_exp_f32_e32 v56, v22
	v_exp_f32_e32 v57, v23
	v_exp_f32_e32 v58, v24
	v_exp_f32_e32 v59, v25
	v_exp_f32_e32 v60, v26
	v_exp_f32_e32 v61, v27
	v_exp_f32_e32 v62, v28
	v_exp_f32_e32 v63, v29
	v_exp_f32_e32 v64, v30
	v_exp_f32_e32 v65, v31
	v_exp_f32_e32 v82, v32
	v_exp_f32_e32 v83, v33
	v_exp_f32_e32 v85, v38
	v_exp_f32_e32 v94, v39
	v_exp_f32_e32 v95, v40
	v_exp_f32_e32 v96, v41
	v_exp_f32_e32 v97, v42
	v_exp_f32_e32 v130, v43
	v_exp_f32_e32 v131, v44
	v_exp_f32_e32 v132, v45
	v_exp_f32_e32 v133, v46
	v_exp_f32_e32 v146, v47
	v_exp_f32_e32 v147, v48
	v_exp_f32_e32 v148, v49
	ds_read_b128 v[22:25], v194 offset:8192
	ds_read_b128 v[26:29], v194 offset:8704
	ds_read_b128 v[30:33], v194 offset:10240
	ds_read_b128 v[38:41], v194 offset:10752
	ds_read_b128 v[42:45], v194 offset:12288
	ds_read_b128 v[46:49], v194 offset:12800
	ds_read_b128 v[86:89], v194 offset:14336
	ds_read_b128 v[90:93], v194 offset:14848
	v_exp_f32_e32 v54, v20
	v_exp_f32_e32 v55, v21
	v_exp_f32_e32 v84, v37
	s_waitcnt vmcnt(2) lgkmcnt(0)
	s_barrier
	v_cmp_gt_u32_e64 s[0:1], 32, v184
	v_exp_f32_e32 v149, v50
	v_exp_f32_e32 v150, v51
	v_exp_f32_e32 v151, v36
	ds_read_b64_tr_b16 v[18:19], v192 offset:24576
	ds_read_b64_tr_b16 v[20:21], v192 offset:25088
	s_waitcnt lgkmcnt(9)
	v_mfma_f32_32x32x16_bf16 v[98:113], v[22:25], v[142:145], v[2:17]
	v_add_f32_e32 v34, v52, v53
	v_add_f32_e32 v34, v34, v54
	v_add_f32_e32 v34, v34, v55
	v_add_f32_e32 v34, v34, v56
	v_add_f32_e32 v50, v34, v57
	v_cvt_pk_bf16_f32 v118, v52, v53
	v_cvt_pk_bf16_f32 v119, v54, v55
	ds_read_b64_tr_b16 v[34:35], v192 offset:28672
	ds_read_b64_tr_b16 v[36:37], v192 offset:29184
	s_waitcnt lgkmcnt(10)
	v_mfma_f32_32x32x16_bf16 v[66:81], v[26:29], v[142:145], v[2:17]
	v_add_f32_e32 v22, v58, v50
	v_add_f32_e32 v22, v59, v22
	v_add_f32_e32 v22, v60, v22
	v_add_f32_e32 v22, v61, v22
	v_cvt_pk_bf16_f32 v120, v56, v57
	v_cvt_pk_bf16_f32 v121, v58, v59
	ds_read_b64_tr_b16 v[50:51], v192 offset:25600
	ds_read_b64_tr_b16 v[52:53], v192 offset:26112
	s_waitcnt lgkmcnt(11)
	v_mfma_f32_32x32x16_bf16 v[98:113], v[30:33], v[138:141], v[98:113]
	v_add_f32_e32 v22, v62, v22
	v_add_f32_e32 v22, v63, v22
	v_add_f32_e32 v22, v64, v22
	v_add_f32_e32 v22, v65, v22
	v_cvt_pk_bf16_f32 v114, v60, v61
	v_cvt_pk_bf16_f32 v115, v62, v63
	ds_read_b64_tr_b16 v[54:55], v192 offset:29696
	ds_read_b64_tr_b16 v[56:57], v192 offset:30208
	s_waitcnt lgkmcnt(12)
	v_mfma_f32_32x32x16_bf16 v[66:81], v[38:41], v[138:141], v[66:81]
	v_add_f32_e32 v22, v82, v22
	v_add_f32_e32 v22, v83, v22
	v_add_f32_e32 v22, v84, v22
	v_add_f32_e32 v22, v85, v22
	v_cvt_pk_bf16_f32 v116, v64, v65
	v_cvt_pk_bf16_f32 v117, v82, v83
	ds_read_b64_tr_b16 v[58:59], v192 offset:26624
	ds_read_b64_tr_b16 v[60:61], v192 offset:27136
	s_waitcnt lgkmcnt(13)
	v_mfma_f32_32x32x16_bf16 v[98:113], v[42:45], v[134:137], v[98:113]
	v_add_f32_e32 v22, v94, v22
	v_add_f32_e32 v22, v95, v22
	v_add_f32_e32 v22, v96, v22
	v_add_f32_e32 v22, v97, v22
	v_cvt_pk_bf16_f32 v122, v84, v85
	v_cvt_pk_bf16_f32 v123, v94, v95
	ds_read_b64_tr_b16 v[62:63], v192 offset:30720
	ds_read_b64_tr_b16 v[64:65], v192 offset:31232
	s_waitcnt lgkmcnt(14)
	v_mfma_f32_32x32x16_bf16 v[66:81], v[46:49], v[134:137], v[66:81]
	v_add_f32_e32 v22, v130, v22
	v_add_f32_e32 v22, v131, v22
	v_add_f32_e32 v22, v132, v22
	v_add_f32_e32 v22, v133, v22
	v_cvt_pk_bf16_f32 v124, v96, v97
	v_cvt_pk_bf16_f32 v125, v130, v131
	ds_read_b64_tr_b16 v[82:83], v192 offset:27648
	ds_read_b64_tr_b16 v[84:85], v192 offset:28160
	s_waitcnt lgkmcnt(14)
	v_mfma_f32_32x32x16_bf16 v[98:113], v[86:89], v[126:129], v[98:113]
	v_add_f32_e32 v22, v146, v22
	v_add_f32_e32 v22, v147, v22
	v_add_f32_e32 v22, v148, v22
	v_add_f32_e32 v22, v149, v22
	v_cvt_pk_bf16_f32 v130, v132, v133
	v_cvt_pk_bf16_f32 v131, v146, v147
	ds_read_b64_tr_b16 v[86:87], v192 offset:31744
	ds_read_b64_tr_b16 v[88:89], v192 offset:32256
	v_mfma_f32_32x32x16_bf16 v[66:81], v[90:93], v[126:129], v[66:81]
	v_add_f32_e32 v22, v150, v22
	v_add_f32_e32 v22, v151, v22
	v_cvt_pk_bf16_f32 v132, v148, v149
	v_cvt_pk_bf16_f32 v133, v150, v151
	s_nop 0
	v_add_f32_e32 v195, 0, v22
	v_lshl_add_u64 v[22:23], v[182:183], 0, s[24:25]
	s_add_i32 s4, s4, 0xa000
	s_mov_b32 s5, m0
	s_mov_b32 m0, s4
	s_nop 0
	global_load_lds_dwordx4 v[22:23], off
	s_mov_b32 m0, s5
	v_max_f32_e32 v22, v98, v99
	v_max3_f32 v23, v100, v101, v67
	v_max3_f32 v22, v22, v66, v68
	v_max3_f32 v22, v22, v69, v102
	v_max3_f32 v23, v23, v104, v105
	v_max3_f32 v22, v22, v103, v70
	v_max3_f32 v23, v23, v72, v73
	v_max3_f32 v22, v22, v71, v106
	v_max3_f32 v23, v23, v108, v109
	v_max3_f32 v22, v22, v107, v74
	v_max3_f32 v23, v23, v76, v77
	v_max3_f32 v22, v22, v75, v110
	v_max3_f32 v23, v23, v112, v113
	v_max3_f32 v22, v22, v111, v78
	v_max3_f32 v23, v23, v80, v81
	v_max3_f32 v22, v22, v79, v23
	v_mov_b32_e32 v23, v22
	s_nop 1
	v_permlane32_swap_b32_e32 v22, v23
	v_max_f32_e32 v22, v22, v23
	v_cmp_lt_f32_e32 vcc, s22, v22
	s_cmp_lg_u64 vcc, 0
	s_cselect_b64 s[4:5], -1, 0
	s_cbranch_vccnz .LBB0_2226

.LBB0_1283:
	ds_read_b64_tr_b16 v[150:151], v192 offset:32768
	ds_read_b64_tr_b16 v[152:153], v192 offset:33280
	s_waitcnt lgkmcnt(9)
	v_mfma_f32_32x32x16_bf16 v[82:97], v[146:149], v[142:145], v[2:17]
	v_add_f32_e32 v50, v98, v99
	v_add_f32_e32 v50, v100, v50
	v_add_f32_e32 v50, v101, v50
	v_add_f32_e32 v50, v102, v50
	v_add_f32_e32 v50, v103, v50
	v_cvt_pk_bf16_f32 v118, v98, v99
	v_cvt_pk_bf16_f32 v119, v100, v101
	ds_read_b64_tr_b16 v[146:147], v192 offset:36864
	ds_read_b64_tr_b16 v[148:149], v192 offset:37376
	v_add_f32_e32 v50, v104, v50
	v_add_f32_e32 v50, v105, v50
	v_add_f32_e32 v50, v106, v50
	v_add_f32_e32 v114, v107, v50
	s_waitcnt lgkmcnt(10)
	v_mfma_f32_32x32x16_bf16 v[50:65], v[174:177], v[142:145], v[2:17]
	v_cvt_pk_bf16_f32 v120, v102, v103
	v_cvt_pk_bf16_f32 v121, v104, v105
	ds_read_b64_tr_b16 v[98:99], v192 offset:33792
	ds_read_b64_tr_b16 v[100:101], v192 offset:34304
	s_waitcnt lgkmcnt(11)
	v_mfma_f32_32x32x16_bf16 v[82:97], v[178:181], v[138:141], v[82:97]
	v_add_f32_e32 v102, v108, v114
	v_add_f32_e32 v102, v109, v102
	v_add_f32_e32 v102, v110, v102
	v_add_f32_e32 v122, v111, v102
	v_cvt_pk_bf16_f32 v114, v106, v107
	v_cvt_pk_bf16_f32 v115, v108, v109
	ds_read_b64_tr_b16 v[102:103], v192 offset:37888
	ds_read_b64_tr_b16 v[104:105], v192 offset:38400
	s_waitcnt lgkmcnt(12)
	v_mfma_f32_32x32x16_bf16 v[50:65], v[170:173], v[138:141], v[50:65]
	v_add_f32_e32 v106, v112, v122
	v_add_f32_e32 v106, v113, v106
	v_add_f32_e32 v106, v66, v106
	v_add_f32_e32 v122, v67, v106
	v_cvt_pk_bf16_f32 v116, v110, v111
	v_cvt_pk_bf16_f32 v117, v112, v113
	ds_read_b64_tr_b16 v[106:107], v192 offset:34816
	ds_read_b64_tr_b16 v[108:109], v192 offset:35328
	s_waitcnt lgkmcnt(13)
	v_mfma_f32_32x32x16_bf16 v[82:97], v[166:169], v[134:137], v[82:97]
	v_add_f32_e32 v110, v68, v122
	v_add_f32_e32 v110, v69, v110
	v_add_f32_e32 v110, v70, v110
	v_add_f32_e32 v110, v71, v110
	v_cvt_pk_bf16_f32 v122, v66, v67
	v_cvt_pk_bf16_f32 v123, v68, v69
	ds_read_b64_tr_b16 v[66:67], v192 offset:38912
	ds_read_b64_tr_b16 v[68:69], v192 offset:39424
	s_waitcnt lgkmcnt(14)
	v_mfma_f32_32x32x16_bf16 v[50:65], v[162:165], v[134:137], v[50:65]
	v_add_f32_e32 v110, v72, v110
	v_add_f32_e32 v110, v73, v110
	v_add_f32_e32 v110, v74, v110
	v_add_f32_e32 v110, v75, v110
	v_cvt_pk_bf16_f32 v124, v70, v71
	v_cvt_pk_bf16_f32 v125, v72, v73
	ds_read_b64_tr_b16 v[70:71], v192 offset:35840
	ds_read_b64_tr_b16 v[72:73], v192 offset:36352
	s_waitcnt lgkmcnt(14)
	v_mfma_f32_32x32x16_bf16 v[82:97], v[158:161], v[126:129], v[82:97]
	v_add_f32_e32 v110, v76, v110
	v_add_f32_e32 v110, v77, v110
	v_add_f32_e32 v110, v78, v110
	v_add_f32_e32 v110, v79, v110
	v_cvt_pk_bf16_f32 v130, v74, v75
	v_cvt_pk_bf16_f32 v131, v76, v77
	ds_read_b64_tr_b16 v[74:75], v192 offset:39936
	ds_read_b64_tr_b16 v[76:77], v192 offset:40448
	v_mfma_f32_32x32x16_bf16 v[50:65], v[154:157], v[126:129], v[50:65]
	v_add_f32_e32 v110, v80, v110
	v_add_f32_e32 v110, v81, v110
	v_cvt_pk_bf16_f32 v132, v78, v79
	v_cvt_pk_bf16_f32 v133, v80, v81
	s_mov_b64 s[4:5], 0xc000
	v_lshl_add_u64 v[78:79], v[182:183], 0, s[4:5]
	s_mov_b32 s4, m0
	s_mov_b32 m0, s11
	s_nop 0
	global_load_lds_dwordx4 v[78:79], off
	s_mov_b32 m0, s4
	v_max_f32_e32 v78, v82, v83
	s_nop 1
	v_max3_f32 v79, v84, v85, v51
	v_max3_f32 v78, v78, v50, v52
	v_max3_f32 v78, v78, v53, v86
	v_max3_f32 v79, v79, v88, v89
	v_max3_f32 v78, v78, v87, v54
	v_max3_f32 v79, v79, v56, v57
	v_max3_f32 v78, v78, v55, v90
	v_max3_f32 v79, v79, v92, v93
	v_max3_f32 v78, v78, v91, v58
	v_max3_f32 v79, v79, v60, v61
	v_max3_f32 v78, v78, v59, v94
	v_max3_f32 v79, v79, v96, v97
	v_max3_f32 v78, v78, v95, v62
	v_max3_f32 v79, v79, v64, v65
	v_max3_f32 v78, v78, v63, v79
	v_mov_b32_e32 v79, v78
	s_nop 1
	v_permlane32_swap_b32_e32 v78, v79
	v_max_f32_e32 v78, v78, v79
	v_cmp_lt_f32_e32 vcc, s22, v78
	s_cmp_lg_u64 vcc, 0
	v_add_f32_e32 v170, v195, v110
	s_cselect_b64 s[4:5], -1, 0
	s_cbranch_vccnz .LBB0_2229

.LBB0_1286:
	ds_read_b64_tr_b16 v[98:99], v192 offset:40960
	ds_read_b64_tr_b16 v[100:101], v192 offset:41472
	v_add_f32_e32 v66, v82, v83
	v_add_f32_e32 v66, v84, v66
	v_add_f32_e32 v66, v85, v66
	v_add_f32_e32 v66, v86, v66
	v_add_f32_e32 v106, v87, v66
	s_waitcnt lgkmcnt(9)
	v_mfma_f32_32x32x16_bf16 v[66:81], v[166:169], v[142:145], v[2:17]
	v_cvt_pk_bf16_f32 v118, v82, v83
	v_cvt_pk_bf16_f32 v119, v84, v85
	ds_read_b64_tr_b16 v[82:83], v192 offset:45056
	ds_read_b64_tr_b16 v[84:85], v192 offset:45568
	s_waitcnt lgkmcnt(10)
	v_mfma_f32_32x32x16_bf16 v[2:17], v[162:165], v[142:145], v[2:17]
	v_add_f32_e32 v106, v88, v106
	v_add_f32_e32 v106, v89, v106
	v_add_f32_e32 v106, v90, v106
	v_add_f32_e32 v106, v91, v106
	v_cvt_pk_bf16_f32 v120, v86, v87
	v_cvt_pk_bf16_f32 v121, v88, v89
	ds_read_b64_tr_b16 v[86:87], v192 offset:41984
	ds_read_b64_tr_b16 v[88:89], v192 offset:42496
	s_waitcnt lgkmcnt(11)
	v_mfma_f32_32x32x16_bf16 v[66:81], v[158:161], v[138:141], v[66:81]
	v_add_f32_e32 v106, v92, v106
	v_add_f32_e32 v106, v93, v106
	v_add_f32_e32 v106, v94, v106
	v_add_f32_e32 v106, v95, v106
	v_cvt_pk_bf16_f32 v114, v90, v91
	v_cvt_pk_bf16_f32 v115, v92, v93
	ds_read_b64_tr_b16 v[90:91], v192 offset:46080
	ds_read_b64_tr_b16 v[92:93], v192 offset:46592
	s_waitcnt lgkmcnt(12)
	v_mfma_f32_32x32x16_bf16 v[2:17], v[154:157], v[138:141], v[2:17]
	v_add_f32_e32 v106, v96, v106
	v_add_f32_e32 v106, v97, v106
	v_add_f32_e32 v106, v50, v106
	v_add_f32_e32 v106, v51, v106
	v_cvt_pk_bf16_f32 v116, v94, v95
	v_cvt_pk_bf16_f32 v117, v96, v97
	ds_read_b64_tr_b16 v[94:95], v192 offset:43008
	ds_read_b64_tr_b16 v[96:97], v192 offset:43520
	s_waitcnt lgkmcnt(13)
	v_mfma_f32_32x32x16_bf16 v[66:81], v[102:105], v[134:137], v[66:81]
	v_add_f32_e32 v102, v52, v106
	v_add_f32_e32 v102, v53, v102
	v_add_f32_e32 v102, v54, v102
	v_add_f32_e32 v106, v55, v102
	v_cvt_pk_bf16_f32 v122, v50, v51
	v_cvt_pk_bf16_f32 v123, v52, v53
	ds_read_b64_tr_b16 v[102:103], v192 offset:47104
	ds_read_b64_tr_b16 v[104:105], v192 offset:47616
	s_waitcnt lgkmcnt(14)
	v_mfma_f32_32x32x16_bf16 v[2:17], v[150:153], v[134:137], v[2:17]
	v_add_f32_e32 v50, v56, v106
	v_add_f32_e32 v50, v57, v50
	v_add_f32_e32 v50, v58, v50
	v_add_f32_e32 v50, v59, v50
	v_cvt_pk_bf16_f32 v124, v54, v55
	v_cvt_pk_bf16_f32 v125, v56, v57
	ds_read_b64_tr_b16 v[106:107], v192 offset:44032
	ds_read_b64_tr_b16 v[108:109], v192 offset:44544
	s_waitcnt lgkmcnt(14)
	v_mfma_f32_32x32x16_bf16 v[66:81], v[146:149], v[126:129], v[66:81]
	v_add_f32_e32 v50, v60, v50
	v_add_f32_e32 v50, v61, v50
	v_add_f32_e32 v50, v62, v50
	v_add_f32_e32 v50, v63, v50
	v_cvt_pk_bf16_f32 v130, v58, v59
	v_cvt_pk_bf16_f32 v131, v60, v61
	ds_read_b64_tr_b16 v[134:135], v192 offset:48128
	ds_read_b64_tr_b16 v[136:137], v192 offset:48640
	v_mfma_f32_32x32x16_bf16 v[2:17], v[110:113], v[126:129], v[2:17]
	v_add_f32_e32 v50, v64, v50
	v_add_f32_e32 v50, v65, v50
	v_cvt_pk_bf16_f32 v132, v62, v63
	v_cvt_pk_bf16_f32 v133, v64, v65
	v_max_f32_e32 v51, v66, v67
	s_nop 3
	s_nop 2
	v_max3_f32 v52, v68, v69, v3
	v_max3_f32 v51, v51, v2, v4
	v_max3_f32 v51, v51, v5, v70
	v_max3_f32 v52, v52, v72, v73
	v_max3_f32 v51, v51, v71, v6
	v_max3_f32 v52, v52, v8, v9
	v_max3_f32 v51, v51, v7, v74
	v_max3_f32 v52, v52, v76, v77
	v_max3_f32 v51, v51, v75, v10
	v_max3_f32 v52, v52, v12, v13
	v_max3_f32 v51, v51, v11, v78
	v_max3_f32 v52, v52, v80, v81
	v_max3_f32 v51, v51, v79, v14
	v_max3_f32 v52, v52, v16, v17
	v_add_f32_e32 v110, v170, v50
	v_max3_f32 v50, v51, v15, v52
	v_mov_b32_e32 v51, v50
	s_nop 1
	v_permlane32_swap_b32_e32 v50, v51
	v_max_f32_e32 v50, v50, v51
	v_cmp_lt_f32_e32 vcc, s22, v50
	s_cmp_lg_u64 vcc, 0
	s_cselect_b64 s[4:5], -1, 0
	s_cbranch_vccnz .LBB0_2232
